# baseline (speedup 1.0000x reference)
.Lkf_par_done:
	s_mov_b64 exec, -1
	v_lshlrev_b32_e32 v4, 4, v4
	v_lshlrev_b32_e32 v5, 6, v5
	v_lshl_or_b32 v3, v3, 2, v4
	v_lshlrev_b32_e32 v4, 4, v12
	v_or3_b32 v3, v3, v5, v2
	v_lshlrev_b32_e32 v5, 6, v13
	v_lshl_or_b32 v4, v11, 2, v4
	v_or3_b32 v43, v4, v5, v10
	v_lshlrev_b32_e32 v4, 4, v16
	v_lshlrev_b32_e32 v5, 6, v17
	v_lshl_or_b32 v4, v15, 2, v4
	v_lshlrev_b32_e32 v8, 4, v8
	v_or3_b32 v42, v4, v5, v14
	v_lshlrev_b32_e32 v4, 4, v20
	v_lshlrev_b32_e32 v9, 6, v9
	v_lshl_or_b32 v7, v7, 2, v8
	v_lshlrev_b32_e32 v5, 6, v21
	v_lshl_or_b32 v4, v19, 2, v4
	v_or3_b32 v44, v7, v9, v6
	v_or3_b32 v41, v4, v5, v18
	v_lshlrev_b32_e32 v4, 4, v24
	v_mov_b32_e32 v7, 0
	v_mov_b32_e32 v8, 0x64c
	v_lshlrev_b32_e32 v5, 6, v25
	v_lshl_or_b32 v4, v23, 2, v4
	s_waitcnt lgkmcnt(0)
	s_barrier
	ds_read_b96 v[36:38], v7 offset:1600
	ds_read_b64 v[16:17], v7 offset:1624
	ds_read2_b32 v[20:21], v8 offset1:1
	v_or3_b32 v19, v4, v5, v22
	v_lshlrev_b32_e32 v4, 4, v28
	v_lshlrev_b32_e32 v5, 6, v29
	v_lshl_or_b32 v4, v27, 2, v4
	v_or3_b32 v13, v4, v5, v26
	v_lshlrev_b32_e32 v4, 4, v32
	v_lshlrev_b32_e32 v5, 6, v33
	v_lshl_or_b32 v4, v31, 2, v4
	v_or3_b32 v9, v4, v5, v30
	s_waitcnt lgkmcnt(0)
	v_pk_fma_f32 v[4:5], v[76:77], v[20:21], v[16:17] op_sel_hi:[1,0,0]
	ds_read_b32 v8, v7 offset:1620
	ds_read_b32 v12, v7 offset:1632
	v_pk_fma_f32 v[4:5], v[78:79], v[36:37], v[4:5] op_sel_hi:[1,0,1]
	v_and_b32_e32 v6, 3, v6
	v_exp_f32_e32 v4, v4
	v_exp_f32_e32 v7, v5
	s_movk_i32 s3, 0xfff
	v_cmp_eq_u32_e32 vcc, 1, v6
	ds_read_b128 v[32:35], v134 offset:49152
	v_cvt_pknorm_u16_f32 v5, v4, v7
	v_lshrrev_b32_e32 v11, 4, v5
	v_bfe_u32 v15, v5, 4, 12
	v_bitop3_b32 v11, v11, s3, v11 bitop3:0xc
	v_cndmask_b32_e32 v15, v15, v11, vcc
	v_mov_b32_e32 v11, 0x670
	v_lshl_add_u32 v25, v15, 2, v11
	v_mov_b32_e32 v15, 0x10000
	v_cndmask_b32_e32 v27, 1, v15, vcc
	v_bfe_u32 v23, v44, 2, 2
	ds_add_u32 v25, v27
	v_cndmask_b32_e32 v25, 0, v4, vcc
	v_lshrrev_b32_e32 v4, 20, v5
	v_xor_b32_e32 v5, 0xfff, v4
	v_cmp_eq_u32_e32 vcc, 1, v23
	v_mov_b32_e32 v24, v38
	s_nop 0
	v_cndmask_b32_e32 v4, v4, v5, vcc
	v_lshl_add_u32 v27, v4, 2, v11
	v_pk_fma_f32 v[4:5], v[76:77], v[20:21], v[16:17] op_sel:[0,1,1]
	v_cndmask_b32_e32 v7, 0, v7, vcc
	v_pk_fma_f32 v[4:5], v[78:79], v[36:37], v[4:5] op_sel:[0,1,0]
	s_nop 0
	v_exp_f32_e32 v4, v4
	v_exp_f32_e32 v28, v5
	v_cndmask_b32_e32 v5, 1, v15, vcc
	ds_add_u32 v27, v5
	v_cmp_eq_u32_e32 vcc, 2, v6
	v_cvt_pknorm_u16_f32 v5, v4, v28
	v_lshrrev_b32_e32 v27, 4, v5
	v_bfe_u32 v29, v5, 4, 12
	v_bitop3_b32 v27, v27, s3, v27 bitop3:0xc
	v_cndmask_b32_e32 v25, v25, v4, vcc
	v_lshrrev_b32_e32 v4, 20, v5
	v_cndmask_b32_e32 v27, v29, v27, vcc
	v_cndmask_b32_e32 v29, 1, v15, vcc
	v_xor_b32_e32 v5, 0xfff, v4
	v_cmp_eq_u32_e32 vcc, 2, v23
	v_lshl_add_u32 v27, v27, 2, v11
	ds_add_u32 v27, v29 offset:16384
	v_cndmask_b32_e32 v4, v4, v5, vcc
	v_lshl_add_u32 v27, v4, 2, v11
	s_waitcnt lgkmcnt(4)
	v_pk_fma_f32 v[4:5], v[76:77], v[8:9], v[12:13] op_sel_hi:[1,0,0]
	v_cndmask_b32_e32 v29, 1, v15, vcc
	v_pk_fma_f32 v[4:5], v[78:79], v[24:25], v[4:5] op_sel_hi:[1,0,1]
	ds_add_u32 v27, v29 offset:16384
	v_exp_f32_e32 v4, v4
	v_exp_f32_e32 v5, v5
	v_cndmask_b32_e32 v7, v7, v28, vcc
	v_cmp_eq_u32_e32 vcc, 3, v6
	v_cvt_pknorm_u16_f32 v27, v4, v5
	v_lshrrev_b32_e32 v28, 4, v27
	v_bfe_u32 v29, v27, 4, 12
	v_bitop3_b32 v28, v28, s3, v28 bitop3:0xc
	v_cndmask_b32_e32 v6, v29, v28, vcc
	v_lshl_add_u32 v6, v6, 2, v11
	v_cndmask_b32_e32 v28, 1, v15, vcc
	ds_add_u32 v6, v28 offset:32768
	v_lshrrev_b32_e32 v6, 20, v27
	v_cndmask_b32_e32 v4, v25, v4, vcc
	v_xor_b32_e32 v25, 0xfff, v6
	v_cmp_eq_u32_e32 vcc, 3, v23
	v_bfe_u32 v27, v44, 6, 2
	s_nop 0
	v_cndmask_b32_e32 v6, v6, v25, vcc
	v_lshl_add_u32 v6, v6, 2, v11
	v_cndmask_b32_e32 v23, 1, v15, vcc
	ds_add_u32 v6, v23 offset:32768
	v_cndmask_b32_e32 v5, v7, v5, vcc
	v_pk_fma_f32 v[6:7], v[20:21], v[80:81], v[16:17] op_sel_hi:[0,1,0]
	v_pk_fma_f32 v[6:7], v[36:37], v[82:83], v[6:7] op_sel_hi:[0,1,1]
	v_exp_f32_e32 v6, v6
	v_exp_f32_e32 v23, v7
	v_bfe_u32 v25, v44, 4, 2
	v_cmp_eq_u32_e32 vcc, 1, v25
	s_waitcnt lgkmcnt(6)
	v_pk_add_f32 v[4:5], v[32:33], v[4:5] neg_lo:[0,1] neg_hi:[0,1]
	v_cvt_pknorm_u16_f32 v7, v6, v23
	v_lshrrev_b32_e32 v28, 4, v7
	v_bfe_u32 v29, v7, 4, 12
	v_bitop3_b32 v28, v28, s3, v28 bitop3:0xc
	v_cndmask_b32_e32 v28, v29, v28, vcc
	v_lshl_add_u32 v28, v28, 2, v11
	v_cndmask_b32_e32 v29, 1, v15, vcc
	ds_add_u32 v28, v29
	v_cndmask_b32_e32 v28, 0, v6, vcc
	v_lshrrev_b32_e32 v6, 20, v7
	v_xor_b32_e32 v7, 0xfff, v6
	v_cmp_eq_u32_e32 vcc, 1, v27
	s_nop 1
	v_cndmask_b32_e32 v6, v6, v7, vcc
	v_lshl_add_u32 v29, v6, 2, v11
	v_pk_fma_f32 v[6:7], v[20:21], v[80:81], v[16:17] op_sel:[1,0,1]
	v_cndmask_b32_e32 v23, 0, v23, vcc
	v_pk_fma_f32 v[6:7], v[36:37], v[82:83], v[6:7] op_sel:[1,0,0]
	s_nop 0
	v_exp_f32_e32 v6, v6
	v_exp_f32_e32 v31, v7
	v_cndmask_b32_e32 v7, 1, v15, vcc
	ds_add_u32 v29, v7
	v_cmp_eq_u32_e32 vcc, 2, v25
	v_cvt_pknorm_u16_f32 v7, v6, v31
	v_lshrrev_b32_e32 v29, 4, v7
	v_bfe_u32 v32, v7, 4, 12
	v_bitop3_b32 v29, v29, s3, v29 bitop3:0xc
	v_cndmask_b32_e32 v28, v28, v6, vcc
	v_lshrrev_b32_e32 v6, 20, v7
	v_cndmask_b32_e32 v29, v32, v29, vcc
	v_cndmask_b32_e32 v32, 1, v15, vcc
	v_xor_b32_e32 v7, 0xfff, v6
	v_cmp_eq_u32_e32 vcc, 2, v27
	v_lshl_add_u32 v29, v29, 2, v11
	ds_add_u32 v29, v32 offset:16384
	v_cndmask_b32_e32 v6, v6, v7, vcc
	v_lshl_add_u32 v29, v6, 2, v11
	v_pk_fma_f32 v[6:7], v[8:9], v[80:81], v[12:13] op_sel_hi:[0,1,0]
	v_pk_fma_f32 v[6:7], v[24:25], v[82:83], v[6:7] op_sel_hi:[0,1,1]
	v_exp_f32_e32 v6, v6
	v_exp_f32_e32 v7, v7
	v_cndmask_b32_e32 v32, 1, v15, vcc
	ds_add_u32 v29, v32 offset:16384
	v_cndmask_b32_e32 v23, v23, v31, vcc
	v_cvt_pknorm_u16_f32 v29, v6, v7
	v_lshrrev_b32_e32 v31, 4, v29
	v_bfe_u32 v32, v29, 4, 12
	v_bitop3_b32 v31, v31, s3, v31 bitop3:0xc
	v_cmp_eq_u32_e32 vcc, 3, v25
	s_nop 1
	v_cndmask_b32_e32 v25, v32, v31, vcc
	v_lshl_add_u32 v25, v25, 2, v11
	v_cndmask_b32_e32 v31, 1, v15, vcc
	ds_add_u32 v25, v31 offset:32768
	v_lshrrev_b32_e32 v25, 20, v29
	v_cndmask_b32_e32 v6, v28, v6, vcc
	v_xor_b32_e32 v28, 0xfff, v25
	v_cmp_eq_u32_e32 vcc, 3, v27
	s_nop 1
	v_cndmask_b32_e32 v25, v25, v28, vcc
	v_lshl_add_u32 v25, v25, 2, v11
	v_cndmask_b32_e32 v27, 1, v15, vcc
	ds_add_u32 v25, v27 offset:32768
	v_cndmask_b32_e32 v7, v23, v7, vcc
	v_pk_add_f32 v[6:7], v[34:35], v[6:7] neg_lo:[0,1] neg_hi:[0,1]
	s_nop 0
	v_pk_mul_f32 v[6:7], v[6:7], v[6:7]
	s_nop 0
	v_pk_fma_f32 v[28:29], v[4:5], v[4:5], v[6:7]
	ds_read_b128 v[76:79], v134 offset:61440
	v_mov_b32_e32 v164, 1
	v_mov_b32_e32 v165, 2
	v_mov_b32_e32 v150, 0
	v_mov_b32_e32 v151, 0
	v_mov_b32_e32 v152, 0
	v_mov_b32_e32 v153, 0
	v_and_b32_e32 v154, 3, v3
	v_bfe_u32 v155, v3, 2, 2
	v_bfe_u32 v156, v3, 4, 2
	v_bfe_u32 v157, v3, 6, 2
	s_mov_b32 s16, 0xfff0fff0
	s_movk_i32 s17, 0x3ffc
	v_pk_fma_f32 v[80:81], v[84:85], v[20:21], v[16:17] op_sel_hi:[1,0,0]
	v_pk_fma_f32 v[80:81], v[86:87], v[36:37], v[80:81] op_sel_hi:[1,0,1]
	s_nop 0
	v_exp_f32_e32 v82, v80
	v_exp_f32_e32 v83, v81
	s_nop 0
	v_cvt_pknorm_u16_f32 v158, v82, v83
	v_and_b32_e32 v159, s16, v158
	v_lshrrev_b32_sdwa v160, v165, v159 dst_sel:DWORD dst_unused:UNUSED_PAD src0_sel:DWORD src1_sel:WORD_0
	v_lshrrev_b32_sdwa v161, v165, v159 dst_sel:DWORD dst_unused:UNUSED_PAD src0_sel:DWORD src1_sel:WORD_1
	v_xor_b32_e32 v162, s17, v160
	v_xor_b32_e32 v163, s17, v161
	v_cmp_ne_u32_e32 vcc, 1, v154
	s_mov_b64 exec, vcc
	ds_add_u32 v160, v164 offset:1648
	s_not_b64 exec, vcc
	ds_add_u32 v162, v15 offset:1648
	v_mov_b32_e32 v150, v82
	s_mov_b64 exec, -1
	v_cmp_ne_u32_e32 vcc, 1, v155
	s_mov_b64 exec, vcc
	ds_add_u32 v161, v164 offset:1648
	s_not_b64 exec, vcc
	ds_add_u32 v163, v15 offset:1648
	v_mov_b32_e32 v151, v83
	s_mov_b64 exec, -1
	v_pk_fma_f32 v[80:81], v[84:85], v[20:21], v[16:17] op_sel:[0,1,1]
	v_pk_fma_f32 v[80:81], v[86:87], v[36:37], v[80:81] op_sel:[0,1,0]
	s_nop 0
	v_exp_f32_e32 v82, v80
	v_exp_f32_e32 v83, v81
	s_nop 0
	v_cvt_pknorm_u16_f32 v158, v82, v83
	v_and_b32_e32 v159, s16, v158
	v_lshrrev_b32_sdwa v160, v165, v159 dst_sel:DWORD dst_unused:UNUSED_PAD src0_sel:DWORD src1_sel:WORD_0
	v_lshrrev_b32_sdwa v161, v165, v159 dst_sel:DWORD dst_unused:UNUSED_PAD src0_sel:DWORD src1_sel:WORD_1
	v_xor_b32_e32 v162, s17, v160
	v_xor_b32_e32 v163, s17, v161
	v_cmp_ne_u32_e32 vcc, 2, v154
	s_mov_b64 exec, vcc
	ds_add_u32 v160, v164 offset:18032
	s_not_b64 exec, vcc
	ds_add_u32 v162, v15 offset:18032
	v_mov_b32_e32 v150, v82
	s_mov_b64 exec, -1
	v_cmp_ne_u32_e32 vcc, 2, v155
	s_mov_b64 exec, vcc
	ds_add_u32 v161, v164 offset:18032
	s_not_b64 exec, vcc
	ds_add_u32 v163, v15 offset:18032
	v_mov_b32_e32 v151, v83
	s_mov_b64 exec, -1
	v_pk_fma_f32 v[80:81], v[84:85], v[8:9], v[12:13] op_sel_hi:[1,0,0]
	v_pk_fma_f32 v[80:81], v[86:87], v[24:25], v[80:81] op_sel_hi:[1,0,1]
	s_nop 0
	v_exp_f32_e32 v82, v80
	v_exp_f32_e32 v83, v81
	s_nop 0
	v_cvt_pknorm_u16_f32 v158, v82, v83
	v_and_b32_e32 v159, s16, v158
	v_lshrrev_b32_sdwa v160, v165, v159 dst_sel:DWORD dst_unused:UNUSED_PAD src0_sel:DWORD src1_sel:WORD_0
	v_lshrrev_b32_sdwa v161, v165, v159 dst_sel:DWORD dst_unused:UNUSED_PAD src0_sel:DWORD src1_sel:WORD_1
	v_xor_b32_e32 v162, s17, v160
	v_xor_b32_e32 v163, s17, v161
	v_cmp_ne_u32_e32 vcc, 3, v154
	s_mov_b64 exec, vcc
	ds_add_u32 v160, v164 offset:34416
	s_not_b64 exec, vcc
	ds_add_u32 v162, v15 offset:34416
	v_mov_b32_e32 v150, v82
	s_mov_b64 exec, -1
	v_cmp_ne_u32_e32 vcc, 3, v155
	s_mov_b64 exec, vcc
	ds_add_u32 v161, v164 offset:34416
	s_not_b64 exec, vcc
	ds_add_u32 v163, v15 offset:34416
	v_mov_b32_e32 v151, v83
	s_mov_b64 exec, -1
	s_waitcnt lgkmcnt(12)
	v_pk_add_f32 v[166:167], v[76:77], v[150:151] neg_lo:[0,1] neg_hi:[0,1]
	s_nop 0
	v_pk_fma_f32 v[166:167], v[166:167], v[166:167], v[28:29]
	v_pk_fma_f32 v[80:81], v[88:89], v[20:21], v[16:17] op_sel_hi:[1,0,0]
	v_pk_fma_f32 v[80:81], v[90:91], v[36:37], v[80:81] op_sel_hi:[1,0,1]
	s_nop 0
	v_exp_f32_e32 v82, v80
	v_exp_f32_e32 v83, v81
	s_nop 0
	v_cvt_pknorm_u16_f32 v158, v82, v83
	v_and_b32_e32 v159, s16, v158
	v_lshrrev_b32_sdwa v160, v165, v159 dst_sel:DWORD dst_unused:UNUSED_PAD src0_sel:DWORD src1_sel:WORD_0
	v_lshrrev_b32_sdwa v161, v165, v159 dst_sel:DWORD dst_unused:UNUSED_PAD src0_sel:DWORD src1_sel:WORD_1
	v_xor_b32_e32 v162, s17, v160
	v_xor_b32_e32 v163, s17, v161
	v_cmp_ne_u32_e32 vcc, 1, v156
	s_mov_b64 exec, vcc
	ds_add_u32 v160, v164 offset:1648
	s_not_b64 exec, vcc
	ds_add_u32 v162, v15 offset:1648
	v_mov_b32_e32 v152, v82
	s_mov_b64 exec, -1
	v_cmp_ne_u32_e32 vcc, 1, v157
	s_mov_b64 exec, vcc
	ds_add_u32 v161, v164 offset:1648
	s_not_b64 exec, vcc
	ds_add_u32 v163, v15 offset:1648
	v_mov_b32_e32 v153, v83
	s_mov_b64 exec, -1
	v_pk_fma_f32 v[80:81], v[88:89], v[20:21], v[16:17] op_sel:[0,1,1]
	v_pk_fma_f32 v[80:81], v[90:91], v[36:37], v[80:81] op_sel:[0,1,0]
	s_nop 0
	v_exp_f32_e32 v82, v80
	v_exp_f32_e32 v83, v81
	s_nop 0
	v_cvt_pknorm_u16_f32 v158, v82, v83
	v_and_b32_e32 v159, s16, v158
	v_lshrrev_b32_sdwa v160, v165, v159 dst_sel:DWORD dst_unused:UNUSED_PAD src0_sel:DWORD src1_sel:WORD_0
	v_lshrrev_b32_sdwa v161, v165, v159 dst_sel:DWORD dst_unused:UNUSED_PAD src0_sel:DWORD src1_sel:WORD_1
	v_xor_b32_e32 v162, s17, v160
	v_xor_b32_e32 v163, s17, v161
	v_cmp_ne_u32_e32 vcc, 2, v156
	s_mov_b64 exec, vcc
	ds_add_u32 v160, v164 offset:18032
	s_not_b64 exec, vcc
	ds_add_u32 v162, v15 offset:18032
	v_mov_b32_e32 v152, v82
	s_mov_b64 exec, -1
	v_cmp_ne_u32_e32 vcc, 2, v157
	s_mov_b64 exec, vcc
	ds_add_u32 v161, v164 offset:18032
	s_not_b64 exec, vcc
	ds_add_u32 v163, v15 offset:18032
	v_mov_b32_e32 v153, v83
	s_mov_b64 exec, -1
	v_pk_fma_f32 v[80:81], v[88:89], v[8:9], v[12:13] op_sel_hi:[1,0,0]
	v_pk_fma_f32 v[80:81], v[90:91], v[24:25], v[80:81] op_sel_hi:[1,0,1]
	s_nop 0
	v_exp_f32_e32 v82, v80
	v_exp_f32_e32 v83, v81
	s_nop 0
	v_cvt_pknorm_u16_f32 v158, v82, v83
	v_and_b32_e32 v159, s16, v158
	v_lshrrev_b32_sdwa v160, v165, v159 dst_sel:DWORD dst_unused:UNUSED_PAD src0_sel:DWORD src1_sel:WORD_0
	v_lshrrev_b32_sdwa v161, v165, v159 dst_sel:DWORD dst_unused:UNUSED_PAD src0_sel:DWORD src1_sel:WORD_1
	v_xor_b32_e32 v162, s17, v160
	v_xor_b32_e32 v163, s17, v161
	v_cmp_ne_u32_e32 vcc, 3, v156
	s_mov_b64 exec, vcc
	ds_add_u32 v160, v164 offset:34416
	s_not_b64 exec, vcc
	ds_add_u32 v162, v15 offset:34416
	v_mov_b32_e32 v152, v82
	s_mov_b64 exec, -1
	v_cmp_ne_u32_e32 vcc, 3, v157
	s_mov_b64 exec, vcc
	ds_add_u32 v161, v164 offset:34416
	s_not_b64 exec, vcc
	ds_add_u32 v163, v15 offset:34416
	v_mov_b32_e32 v153, v83
	s_mov_b64 exec, -1
	v_pk_add_f32 v[80:81], v[78:79], v[152:153] neg_lo:[0,1] neg_hi:[0,1]
	s_nop 0
	v_pk_fma_f32 v[6:7], v[80:81], v[80:81], v[166:167]
	ds_read_b128 v[76:79], v1 offset:24576
	v_mov_b32_e32 v164, 1
	v_mov_b32_e32 v165, 2
	v_mov_b32_e32 v150, 0
	v_mov_b32_e32 v151, 0
	v_mov_b32_e32 v152, 0
	v_mov_b32_e32 v153, 0
	v_and_b32_e32 v154, 3, v43
	v_bfe_u32 v155, v43, 2, 2
	v_bfe_u32 v156, v43, 4, 2
	v_bfe_u32 v157, v43, 6, 2
	s_mov_b32 s16, 0xfff0fff0
	s_movk_i32 s17, 0x3ffc
	v_pk_fma_f32 v[80:81], v[92:93], v[20:21], v[16:17] op_sel_hi:[1,0,0]
	v_pk_fma_f32 v[80:81], v[94:95], v[36:37], v[80:81] op_sel_hi:[1,0,1]
	s_nop 0
	v_exp_f32_e32 v82, v80
	v_exp_f32_e32 v83, v81
	s_nop 0
	v_cvt_pknorm_u16_f32 v158, v82, v83
	v_and_b32_e32 v159, s16, v158
	v_lshrrev_b32_sdwa v160, v165, v159 dst_sel:DWORD dst_unused:UNUSED_PAD src0_sel:DWORD src1_sel:WORD_0
	v_lshrrev_b32_sdwa v161, v165, v159 dst_sel:DWORD dst_unused:UNUSED_PAD src0_sel:DWORD src1_sel:WORD_1
	v_xor_b32_e32 v162, s17, v160
	v_xor_b32_e32 v163, s17, v161
	v_cmp_ne_u32_e32 vcc, 1, v154
	s_mov_b64 exec, vcc
	ds_add_u32 v160, v164 offset:1648
	s_not_b64 exec, vcc
	ds_add_u32 v162, v15 offset:1648
	v_mov_b32_e32 v150, v82
	s_mov_b64 exec, -1
	v_cmp_ne_u32_e32 vcc, 1, v155
	s_mov_b64 exec, vcc
	ds_add_u32 v161, v164 offset:1648
	s_not_b64 exec, vcc
	ds_add_u32 v163, v15 offset:1648
	v_mov_b32_e32 v151, v83
	s_mov_b64 exec, -1
	v_pk_fma_f32 v[80:81], v[92:93], v[20:21], v[16:17] op_sel:[0,1,1]
	v_pk_fma_f32 v[80:81], v[94:95], v[36:37], v[80:81] op_sel:[0,1,0]
	s_nop 0
	v_exp_f32_e32 v82, v80
	v_exp_f32_e32 v83, v81
	s_nop 0
	v_cvt_pknorm_u16_f32 v158, v82, v83
	v_and_b32_e32 v159, s16, v158
	v_lshrrev_b32_sdwa v160, v165, v159 dst_sel:DWORD dst_unused:UNUSED_PAD src0_sel:DWORD src1_sel:WORD_0
	v_lshrrev_b32_sdwa v161, v165, v159 dst_sel:DWORD dst_unused:UNUSED_PAD src0_sel:DWORD src1_sel:WORD_1
	v_xor_b32_e32 v162, s17, v160
	v_xor_b32_e32 v163, s17, v161
	v_cmp_ne_u32_e32 vcc, 2, v154
	s_mov_b64 exec, vcc
	ds_add_u32 v160, v164 offset:18032
	s_not_b64 exec, vcc
	ds_add_u32 v162, v15 offset:18032
	v_mov_b32_e32 v150, v82
	s_mov_b64 exec, -1
	v_cmp_ne_u32_e32 vcc, 2, v155
	s_mov_b64 exec, vcc
	ds_add_u32 v161, v164 offset:18032
	s_not_b64 exec, vcc
	ds_add_u32 v163, v15 offset:18032
	v_mov_b32_e32 v151, v83
	s_mov_b64 exec, -1
	v_pk_fma_f32 v[80:81], v[92:93], v[8:9], v[12:13] op_sel_hi:[1,0,0]
	v_pk_fma_f32 v[80:81], v[94:95], v[24:25], v[80:81] op_sel_hi:[1,0,1]
	s_nop 0
	v_exp_f32_e32 v82, v80
	v_exp_f32_e32 v83, v81
	s_nop 0
	v_cvt_pknorm_u16_f32 v158, v82, v83
	v_and_b32_e32 v159, s16, v158
	v_lshrrev_b32_sdwa v160, v165, v159 dst_sel:DWORD dst_unused:UNUSED_PAD src0_sel:DWORD src1_sel:WORD_0
	v_lshrrev_b32_sdwa v161, v165, v159 dst_sel:DWORD dst_unused:UNUSED_PAD src0_sel:DWORD src1_sel:WORD_1
	v_xor_b32_e32 v162, s17, v160
	v_xor_b32_e32 v163, s17, v161
	v_cmp_ne_u32_e32 vcc, 3, v154
	s_mov_b64 exec, vcc
	ds_add_u32 v160, v164 offset:34416
	s_not_b64 exec, vcc
	ds_add_u32 v162, v15 offset:34416
	v_mov_b32_e32 v150, v82
	s_mov_b64 exec, -1
	v_cmp_ne_u32_e32 vcc, 3, v155
	s_mov_b64 exec, vcc
	ds_add_u32 v161, v164 offset:34416
	s_not_b64 exec, vcc
	ds_add_u32 v163, v15 offset:34416
	v_mov_b32_e32 v151, v83
	s_mov_b64 exec, -1
	s_waitcnt lgkmcnt(12)
	v_pk_add_f32 v[166:167], v[76:77], v[150:151] neg_lo:[0,1] neg_hi:[0,1]
	s_nop 0
	v_pk_fma_f32 v[166:167], v[166:167], v[166:167], v[6:7]
	v_pk_fma_f32 v[80:81], v[96:97], v[20:21], v[16:17] op_sel_hi:[1,0,0]
	v_pk_fma_f32 v[80:81], v[98:99], v[36:37], v[80:81] op_sel_hi:[1,0,1]
	s_nop 0
	v_exp_f32_e32 v82, v80
	v_exp_f32_e32 v83, v81
	s_nop 0
	v_cvt_pknorm_u16_f32 v158, v82, v83
	v_and_b32_e32 v159, s16, v158
	v_lshrrev_b32_sdwa v160, v165, v159 dst_sel:DWORD dst_unused:UNUSED_PAD src0_sel:DWORD src1_sel:WORD_0
	v_lshrrev_b32_sdwa v161, v165, v159 dst_sel:DWORD dst_unused:UNUSED_PAD src0_sel:DWORD src1_sel:WORD_1
	v_xor_b32_e32 v162, s17, v160
	v_xor_b32_e32 v163, s17, v161
	v_cmp_ne_u32_e32 vcc, 1, v156
	s_mov_b64 exec, vcc
	ds_add_u32 v160, v164 offset:1648
	s_not_b64 exec, vcc
	ds_add_u32 v162, v15 offset:1648
	v_mov_b32_e32 v152, v82
	s_mov_b64 exec, -1
	v_cmp_ne_u32_e32 vcc, 1, v157
	s_mov_b64 exec, vcc
	ds_add_u32 v161, v164 offset:1648
	s_not_b64 exec, vcc
	ds_add_u32 v163, v15 offset:1648
	v_mov_b32_e32 v153, v83
	s_mov_b64 exec, -1
	v_pk_fma_f32 v[80:81], v[96:97], v[20:21], v[16:17] op_sel:[0,1,1]
	v_pk_fma_f32 v[80:81], v[98:99], v[36:37], v[80:81] op_sel:[0,1,0]
	s_nop 0
	v_exp_f32_e32 v82, v80
	v_exp_f32_e32 v83, v81
	s_nop 0
	v_cvt_pknorm_u16_f32 v158, v82, v83
	v_and_b32_e32 v159, s16, v158
	v_lshrrev_b32_sdwa v160, v165, v159 dst_sel:DWORD dst_unused:UNUSED_PAD src0_sel:DWORD src1_sel:WORD_0
	v_lshrrev_b32_sdwa v161, v165, v159 dst_sel:DWORD dst_unused:UNUSED_PAD src0_sel:DWORD src1_sel:WORD_1
	v_xor_b32_e32 v162, s17, v160
	v_xor_b32_e32 v163, s17, v161
	v_cmp_ne_u32_e32 vcc, 2, v156
	s_mov_b64 exec, vcc
	ds_add_u32 v160, v164 offset:18032
	s_not_b64 exec, vcc
	ds_add_u32 v162, v15 offset:18032
	v_mov_b32_e32 v152, v82
	s_mov_b64 exec, -1
	v_cmp_ne_u32_e32 vcc, 2, v157
	s_mov_b64 exec, vcc
	ds_add_u32 v161, v164 offset:18032
	s_not_b64 exec, vcc
	ds_add_u32 v163, v15 offset:18032
	v_mov_b32_e32 v153, v83
	s_mov_b64 exec, -1
	v_pk_fma_f32 v[80:81], v[96:97], v[8:9], v[12:13] op_sel_hi:[1,0,0]
	v_pk_fma_f32 v[80:81], v[98:99], v[24:25], v[80:81] op_sel_hi:[1,0,1]
	s_nop 0
	v_exp_f32_e32 v82, v80
	v_exp_f32_e32 v83, v81
	s_nop 0
	v_cvt_pknorm_u16_f32 v158, v82, v83
	v_and_b32_e32 v159, s16, v158
	v_lshrrev_b32_sdwa v160, v165, v159 dst_sel:DWORD dst_unused:UNUSED_PAD src0_sel:DWORD src1_sel:WORD_0
	v_lshrrev_b32_sdwa v161, v165, v159 dst_sel:DWORD dst_unused:UNUSED_PAD src0_sel:DWORD src1_sel:WORD_1
	v_xor_b32_e32 v162, s17, v160
	v_xor_b32_e32 v163, s17, v161
	v_cmp_ne_u32_e32 vcc, 3, v156
	s_mov_b64 exec, vcc
	ds_add_u32 v160, v164 offset:34416
	s_not_b64 exec, vcc
	ds_add_u32 v162, v15 offset:34416
	v_mov_b32_e32 v152, v82
	s_mov_b64 exec, -1
	v_cmp_ne_u32_e32 vcc, 3, v157
	s_mov_b64 exec, vcc
	ds_add_u32 v161, v164 offset:34416
	s_not_b64 exec, vcc
	ds_add_u32 v163, v15 offset:34416
	v_mov_b32_e32 v153, v83
	s_mov_b64 exec, -1
	v_pk_add_f32 v[80:81], v[78:79], v[152:153] neg_lo:[0,1] neg_hi:[0,1]
	s_nop 0
	v_pk_fma_f32 v[6:7], v[80:81], v[80:81], v[166:167]
	ds_read_b128 v[76:79], v1 offset:36864
	v_mov_b32_e32 v164, 1
	v_mov_b32_e32 v165, 2
	v_mov_b32_e32 v150, 0
	v_mov_b32_e32 v151, 0
	v_mov_b32_e32 v152, 0
	v_mov_b32_e32 v153, 0
	v_and_b32_e32 v154, 3, v42
	v_bfe_u32 v155, v42, 2, 2
	v_bfe_u32 v156, v42, 4, 2
	v_bfe_u32 v157, v42, 6, 2
	s_mov_b32 s16, 0xfff0fff0
	s_movk_i32 s17, 0x3ffc
	v_pk_fma_f32 v[80:81], v[100:101], v[20:21], v[16:17] op_sel_hi:[1,0,0]
	v_pk_fma_f32 v[80:81], v[102:103], v[36:37], v[80:81] op_sel_hi:[1,0,1]
	s_nop 0
	v_exp_f32_e32 v82, v80
	v_exp_f32_e32 v83, v81
	s_nop 0
	v_cvt_pknorm_u16_f32 v158, v82, v83
	v_and_b32_e32 v159, s16, v158
	v_lshrrev_b32_sdwa v160, v165, v159 dst_sel:DWORD dst_unused:UNUSED_PAD src0_sel:DWORD src1_sel:WORD_0
	v_lshrrev_b32_sdwa v161, v165, v159 dst_sel:DWORD dst_unused:UNUSED_PAD src0_sel:DWORD src1_sel:WORD_1
	v_xor_b32_e32 v162, s17, v160
	v_xor_b32_e32 v163, s17, v161
	v_cmp_ne_u32_e32 vcc, 1, v154
	s_mov_b64 exec, vcc
	ds_add_u32 v160, v164 offset:1648
	s_not_b64 exec, vcc
	ds_add_u32 v162, v15 offset:1648
	v_mov_b32_e32 v150, v82
	s_mov_b64 exec, -1
	v_cmp_ne_u32_e32 vcc, 1, v155
	s_mov_b64 exec, vcc
	ds_add_u32 v161, v164 offset:1648
	s_not_b64 exec, vcc
	ds_add_u32 v163, v15 offset:1648
	v_mov_b32_e32 v151, v83
	s_mov_b64 exec, -1
	v_pk_fma_f32 v[80:81], v[100:101], v[20:21], v[16:17] op_sel:[0,1,1]
	v_pk_fma_f32 v[80:81], v[102:103], v[36:37], v[80:81] op_sel:[0,1,0]
	s_nop 0
	v_exp_f32_e32 v82, v80
	v_exp_f32_e32 v83, v81
	s_nop 0
	v_cvt_pknorm_u16_f32 v158, v82, v83
	v_and_b32_e32 v159, s16, v158
	v_lshrrev_b32_sdwa v160, v165, v159 dst_sel:DWORD dst_unused:UNUSED_PAD src0_sel:DWORD src1_sel:WORD_0
	v_lshrrev_b32_sdwa v161, v165, v159 dst_sel:DWORD dst_unused:UNUSED_PAD src0_sel:DWORD src1_sel:WORD_1
	v_xor_b32_e32 v162, s17, v160
	v_xor_b32_e32 v163, s17, v161
	v_cmp_ne_u32_e32 vcc, 2, v154
	s_mov_b64 exec, vcc
	ds_add_u32 v160, v164 offset:18032
	s_not_b64 exec, vcc
	ds_add_u32 v162, v15 offset:18032
	v_mov_b32_e32 v150, v82
	s_mov_b64 exec, -1
	v_cmp_ne_u32_e32 vcc, 2, v155
	s_mov_b64 exec, vcc
	ds_add_u32 v161, v164 offset:18032
	s_not_b64 exec, vcc
	ds_add_u32 v163, v15 offset:18032
	v_mov_b32_e32 v151, v83
	s_mov_b64 exec, -1
	v_pk_fma_f32 v[80:81], v[100:101], v[8:9], v[12:13] op_sel_hi:[1,0,0]
	v_pk_fma_f32 v[80:81], v[102:103], v[24:25], v[80:81] op_sel_hi:[1,0,1]
	s_nop 0
	v_exp_f32_e32 v82, v80
	v_exp_f32_e32 v83, v81
	s_nop 0
	v_cvt_pknorm_u16_f32 v158, v82, v83
	v_and_b32_e32 v159, s16, v158
	v_lshrrev_b32_sdwa v160, v165, v159 dst_sel:DWORD dst_unused:UNUSED_PAD src0_sel:DWORD src1_sel:WORD_0
	v_lshrrev_b32_sdwa v161, v165, v159 dst_sel:DWORD dst_unused:UNUSED_PAD src0_sel:DWORD src1_sel:WORD_1
	v_xor_b32_e32 v162, s17, v160
	v_xor_b32_e32 v163, s17, v161
	v_cmp_ne_u32_e32 vcc, 3, v154
	s_mov_b64 exec, vcc
	ds_add_u32 v160, v164 offset:34416
	s_not_b64 exec, vcc
	ds_add_u32 v162, v15 offset:34416
	v_mov_b32_e32 v150, v82
	s_mov_b64 exec, -1
	v_cmp_ne_u32_e32 vcc, 3, v155
	s_mov_b64 exec, vcc
	ds_add_u32 v161, v164 offset:34416
	s_not_b64 exec, vcc
	ds_add_u32 v163, v15 offset:34416
	v_mov_b32_e32 v151, v83
	s_mov_b64 exec, -1
	s_waitcnt lgkmcnt(12)
	v_pk_add_f32 v[166:167], v[76:77], v[150:151] neg_lo:[0,1] neg_hi:[0,1]
	s_nop 0
	v_pk_fma_f32 v[166:167], v[166:167], v[166:167], v[6:7]
	v_pk_fma_f32 v[80:81], v[104:105], v[20:21], v[16:17] op_sel_hi:[1,0,0]
	v_pk_fma_f32 v[80:81], v[106:107], v[36:37], v[80:81] op_sel_hi:[1,0,1]
	s_nop 0
	v_exp_f32_e32 v82, v80
	v_exp_f32_e32 v83, v81
	s_nop 0
	v_cvt_pknorm_u16_f32 v158, v82, v83
	v_and_b32_e32 v159, s16, v158
	v_lshrrev_b32_sdwa v160, v165, v159 dst_sel:DWORD dst_unused:UNUSED_PAD src0_sel:DWORD src1_sel:WORD_0
	v_lshrrev_b32_sdwa v161, v165, v159 dst_sel:DWORD dst_unused:UNUSED_PAD src0_sel:DWORD src1_sel:WORD_1
	v_xor_b32_e32 v162, s17, v160
	v_xor_b32_e32 v163, s17, v161
	v_cmp_ne_u32_e32 vcc, 1, v156
	s_mov_b64 exec, vcc
	ds_add_u32 v160, v164 offset:1648
	s_not_b64 exec, vcc
	ds_add_u32 v162, v15 offset:1648
	v_mov_b32_e32 v152, v82
	s_mov_b64 exec, -1
	v_cmp_ne_u32_e32 vcc, 1, v157
	s_mov_b64 exec, vcc
	ds_add_u32 v161, v164 offset:1648
	s_not_b64 exec, vcc
	ds_add_u32 v163, v15 offset:1648
	v_mov_b32_e32 v153, v83
	s_mov_b64 exec, -1
	v_pk_fma_f32 v[80:81], v[104:105], v[20:21], v[16:17] op_sel:[0,1,1]
	v_pk_fma_f32 v[80:81], v[106:107], v[36:37], v[80:81] op_sel:[0,1,0]
	s_nop 0
	v_exp_f32_e32 v82, v80
	v_exp_f32_e32 v83, v81
	s_nop 0
	v_cvt_pknorm_u16_f32 v158, v82, v83
	v_and_b32_e32 v159, s16, v158
	v_lshrrev_b32_sdwa v160, v165, v159 dst_sel:DWORD dst_unused:UNUSED_PAD src0_sel:DWORD src1_sel:WORD_0
	v_lshrrev_b32_sdwa v161, v165, v159 dst_sel:DWORD dst_unused:UNUSED_PAD src0_sel:DWORD src1_sel:WORD_1
	v_xor_b32_e32 v162, s17, v160
	v_xor_b32_e32 v163, s17, v161
	v_cmp_ne_u32_e32 vcc, 2, v156
	s_mov_b64 exec, vcc
	ds_add_u32 v160, v164 offset:18032
	s_not_b64 exec, vcc
	ds_add_u32 v162, v15 offset:18032
	v_mov_b32_e32 v152, v82
	s_mov_b64 exec, -1
	v_cmp_ne_u32_e32 vcc, 2, v157
	s_mov_b64 exec, vcc
	ds_add_u32 v161, v164 offset:18032
	s_not_b64 exec, vcc
	ds_add_u32 v163, v15 offset:18032
	v_mov_b32_e32 v153, v83
	s_mov_b64 exec, -1
	v_pk_fma_f32 v[80:81], v[104:105], v[8:9], v[12:13] op_sel_hi:[1,0,0]
	v_pk_fma_f32 v[80:81], v[106:107], v[24:25], v[80:81] op_sel_hi:[1,0,1]
	s_nop 0
	v_exp_f32_e32 v82, v80
	v_exp_f32_e32 v83, v81
	s_nop 0
	v_cvt_pknorm_u16_f32 v158, v82, v83
	v_and_b32_e32 v159, s16, v158
	v_lshrrev_b32_sdwa v160, v165, v159 dst_sel:DWORD dst_unused:UNUSED_PAD src0_sel:DWORD src1_sel:WORD_0
	v_lshrrev_b32_sdwa v161, v165, v159 dst_sel:DWORD dst_unused:UNUSED_PAD src0_sel:DWORD src1_sel:WORD_1
	v_xor_b32_e32 v162, s17, v160
	v_xor_b32_e32 v163, s17, v161
	v_cmp_ne_u32_e32 vcc, 3, v156
	s_mov_b64 exec, vcc
	ds_add_u32 v160, v164 offset:34416
	s_not_b64 exec, vcc
	ds_add_u32 v162, v15 offset:34416
	v_mov_b32_e32 v152, v82
	s_mov_b64 exec, -1
	v_cmp_ne_u32_e32 vcc, 3, v157
	s_mov_b64 exec, vcc
	ds_add_u32 v161, v164 offset:34416
	s_not_b64 exec, vcc
	ds_add_u32 v163, v15 offset:34416
	v_mov_b32_e32 v153, v83
	s_mov_b64 exec, -1
	v_pk_add_f32 v[80:81], v[78:79], v[152:153] neg_lo:[0,1] neg_hi:[0,1]
	s_nop 0
	v_pk_fma_f32 v[6:7], v[80:81], v[80:81], v[166:167]
	ds_read_b128 v[76:79], v1 offset:49152
	v_mov_b32_e32 v164, 1
	v_mov_b32_e32 v165, 2
	v_mov_b32_e32 v150, 0
	v_mov_b32_e32 v151, 0
	v_mov_b32_e32 v152, 0
	v_mov_b32_e32 v153, 0
	v_and_b32_e32 v154, 3, v41
	v_bfe_u32 v155, v41, 2, 2
	v_bfe_u32 v156, v41, 4, 2
	v_bfe_u32 v157, v41, 6, 2
	s_mov_b32 s16, 0xfff0fff0
	s_movk_i32 s17, 0x3ffc
	v_pk_fma_f32 v[80:81], v[108:109], v[20:21], v[16:17] op_sel_hi:[1,0,0]
	v_pk_fma_f32 v[80:81], v[110:111], v[36:37], v[80:81] op_sel_hi:[1,0,1]
	s_nop 0
	v_exp_f32_e32 v82, v80
	v_exp_f32_e32 v83, v81
	s_nop 0
	v_cvt_pknorm_u16_f32 v158, v82, v83
	v_and_b32_e32 v159, s16, v158
	v_lshrrev_b32_sdwa v160, v165, v159 dst_sel:DWORD dst_unused:UNUSED_PAD src0_sel:DWORD src1_sel:WORD_0
	v_lshrrev_b32_sdwa v161, v165, v159 dst_sel:DWORD dst_unused:UNUSED_PAD src0_sel:DWORD src1_sel:WORD_1
	v_xor_b32_e32 v162, s17, v160
	v_xor_b32_e32 v163, s17, v161
	v_cmp_ne_u32_e32 vcc, 1, v154
	s_mov_b64 exec, vcc
	ds_add_u32 v160, v164 offset:1648
	s_not_b64 exec, vcc
	ds_add_u32 v162, v15 offset:1648
	v_mov_b32_e32 v150, v82
	s_mov_b64 exec, -1
	v_cmp_ne_u32_e32 vcc, 1, v155
	s_mov_b64 exec, vcc
	ds_add_u32 v161, v164 offset:1648
	s_not_b64 exec, vcc
	ds_add_u32 v163, v15 offset:1648
	v_mov_b32_e32 v151, v83
	s_mov_b64 exec, -1
	v_pk_fma_f32 v[80:81], v[108:109], v[20:21], v[16:17] op_sel:[0,1,1]
	v_pk_fma_f32 v[80:81], v[110:111], v[36:37], v[80:81] op_sel:[0,1,0]
	s_nop 0
	v_exp_f32_e32 v82, v80
	v_exp_f32_e32 v83, v81
	s_nop 0
	v_cvt_pknorm_u16_f32 v158, v82, v83
	v_and_b32_e32 v159, s16, v158
	v_lshrrev_b32_sdwa v160, v165, v159 dst_sel:DWORD dst_unused:UNUSED_PAD src0_sel:DWORD src1_sel:WORD_0
	v_lshrrev_b32_sdwa v161, v165, v159 dst_sel:DWORD dst_unused:UNUSED_PAD src0_sel:DWORD src1_sel:WORD_1
	v_xor_b32_e32 v162, s17, v160
	v_xor_b32_e32 v163, s17, v161
	v_cmp_ne_u32_e32 vcc, 2, v154
	s_mov_b64 exec, vcc
	ds_add_u32 v160, v164 offset:18032
	s_not_b64 exec, vcc
	ds_add_u32 v162, v15 offset:18032
	v_mov_b32_e32 v150, v82
	s_mov_b64 exec, -1
	v_cmp_ne_u32_e32 vcc, 2, v155
	s_mov_b64 exec, vcc
	ds_add_u32 v161, v164 offset:18032
	s_not_b64 exec, vcc
	ds_add_u32 v163, v15 offset:18032
	v_mov_b32_e32 v151, v83
	s_mov_b64 exec, -1
	v_pk_fma_f32 v[80:81], v[108:109], v[8:9], v[12:13] op_sel_hi:[1,0,0]
	v_pk_fma_f32 v[80:81], v[110:111], v[24:25], v[80:81] op_sel_hi:[1,0,1]
	s_nop 0
	v_exp_f32_e32 v82, v80
	v_exp_f32_e32 v83, v81
	s_nop 0
	v_cvt_pknorm_u16_f32 v158, v82, v83
	v_and_b32_e32 v159, s16, v158
	v_lshrrev_b32_sdwa v160, v165, v159 dst_sel:DWORD dst_unused:UNUSED_PAD src0_sel:DWORD src1_sel:WORD_0
	v_lshrrev_b32_sdwa v161, v165, v159 dst_sel:DWORD dst_unused:UNUSED_PAD src0_sel:DWORD src1_sel:WORD_1
	v_xor_b32_e32 v162, s17, v160
	v_xor_b32_e32 v163, s17, v161
	v_cmp_ne_u32_e32 vcc, 3, v154
	s_mov_b64 exec, vcc
	ds_add_u32 v160, v164 offset:34416
	s_not_b64 exec, vcc
	ds_add_u32 v162, v15 offset:34416
	v_mov_b32_e32 v150, v82
	s_mov_b64 exec, -1
	v_cmp_ne_u32_e32 vcc, 3, v155
	s_mov_b64 exec, vcc
	ds_add_u32 v161, v164 offset:34416
	s_not_b64 exec, vcc
	ds_add_u32 v163, v15 offset:34416
	v_mov_b32_e32 v151, v83
	s_mov_b64 exec, -1
	s_waitcnt lgkmcnt(12)
	v_pk_add_f32 v[166:167], v[76:77], v[150:151] neg_lo:[0,1] neg_hi:[0,1]
	s_nop 0
	v_pk_fma_f32 v[166:167], v[166:167], v[166:167], v[6:7]
	v_pk_fma_f32 v[80:81], v[112:113], v[20:21], v[16:17] op_sel_hi:[1,0,0]
	v_pk_fma_f32 v[80:81], v[114:115], v[36:37], v[80:81] op_sel_hi:[1,0,1]
	s_nop 0
	v_exp_f32_e32 v82, v80
	v_exp_f32_e32 v83, v81
	s_nop 0
	v_cvt_pknorm_u16_f32 v158, v82, v83
	v_and_b32_e32 v159, s16, v158
	v_lshrrev_b32_sdwa v160, v165, v159 dst_sel:DWORD dst_unused:UNUSED_PAD src0_sel:DWORD src1_sel:WORD_0
	v_lshrrev_b32_sdwa v161, v165, v159 dst_sel:DWORD dst_unused:UNUSED_PAD src0_sel:DWORD src1_sel:WORD_1
	v_xor_b32_e32 v162, s17, v160
	v_xor_b32_e32 v163, s17, v161
	v_cmp_ne_u32_e32 vcc, 1, v156
	s_mov_b64 exec, vcc
	ds_add_u32 v160, v164 offset:1648
	s_not_b64 exec, vcc
	ds_add_u32 v162, v15 offset:1648
	v_mov_b32_e32 v152, v82
	s_mov_b64 exec, -1
	v_cmp_ne_u32_e32 vcc, 1, v157
	s_mov_b64 exec, vcc
	ds_add_u32 v161, v164 offset:1648
	s_not_b64 exec, vcc
	ds_add_u32 v163, v15 offset:1648
	v_mov_b32_e32 v153, v83
	s_mov_b64 exec, -1
	v_pk_fma_f32 v[80:81], v[112:113], v[20:21], v[16:17] op_sel:[0,1,1]
	v_pk_fma_f32 v[80:81], v[114:115], v[36:37], v[80:81] op_sel:[0,1,0]
	s_nop 0
	v_exp_f32_e32 v82, v80
	v_exp_f32_e32 v83, v81
	s_nop 0
	v_cvt_pknorm_u16_f32 v158, v82, v83
	v_and_b32_e32 v159, s16, v158
	v_lshrrev_b32_sdwa v160, v165, v159 dst_sel:DWORD dst_unused:UNUSED_PAD src0_sel:DWORD src1_sel:WORD_0
	v_lshrrev_b32_sdwa v161, v165, v159 dst_sel:DWORD dst_unused:UNUSED_PAD src0_sel:DWORD src1_sel:WORD_1
	v_xor_b32_e32 v162, s17, v160
	v_xor_b32_e32 v163, s17, v161
	v_cmp_ne_u32_e32 vcc, 2, v156
	s_mov_b64 exec, vcc
	ds_add_u32 v160, v164 offset:18032
	s_not_b64 exec, vcc
	ds_add_u32 v162, v15 offset:18032
	v_mov_b32_e32 v152, v82
	s_mov_b64 exec, -1
	v_cmp_ne_u32_e32 vcc, 2, v157
	s_mov_b64 exec, vcc
	ds_add_u32 v161, v164 offset:18032
	s_not_b64 exec, vcc
	ds_add_u32 v163, v15 offset:18032
	v_mov_b32_e32 v153, v83
	s_mov_b64 exec, -1
	v_pk_fma_f32 v[80:81], v[112:113], v[8:9], v[12:13] op_sel_hi:[1,0,0]
	v_pk_fma_f32 v[80:81], v[114:115], v[24:25], v[80:81] op_sel_hi:[1,0,1]
	s_nop 0
	v_exp_f32_e32 v82, v80
	v_exp_f32_e32 v83, v81
	s_nop 0
	v_cvt_pknorm_u16_f32 v158, v82, v83
	v_and_b32_e32 v159, s16, v158
	v_lshrrev_b32_sdwa v160, v165, v159 dst_sel:DWORD dst_unused:UNUSED_PAD src0_sel:DWORD src1_sel:WORD_0
	v_lshrrev_b32_sdwa v161, v165, v159 dst_sel:DWORD dst_unused:UNUSED_PAD src0_sel:DWORD src1_sel:WORD_1
	v_xor_b32_e32 v162, s17, v160
	v_xor_b32_e32 v163, s17, v161
	v_cmp_ne_u32_e32 vcc, 3, v156
	s_mov_b64 exec, vcc
	ds_add_u32 v160, v164 offset:34416
	s_not_b64 exec, vcc
	ds_add_u32 v162, v15 offset:34416
	v_mov_b32_e32 v152, v82
	s_mov_b64 exec, -1
	v_cmp_ne_u32_e32 vcc, 3, v157
	s_mov_b64 exec, vcc
	ds_add_u32 v161, v164 offset:34416
	s_not_b64 exec, vcc
	ds_add_u32 v163, v15 offset:34416
	v_mov_b32_e32 v153, v83
	s_mov_b64 exec, -1
	v_pk_add_f32 v[80:81], v[78:79], v[152:153] neg_lo:[0,1] neg_hi:[0,1]
	s_nop 0
	v_pk_fma_f32 v[6:7], v[80:81], v[80:81], v[166:167]
	ds_read_b128 v[76:79], v1 offset:61440
	v_mov_b32_e32 v164, 1
	v_mov_b32_e32 v165, 2
	v_mov_b32_e32 v150, 0
	v_mov_b32_e32 v151, 0
	v_mov_b32_e32 v152, 0
	v_mov_b32_e32 v153, 0
	v_and_b32_e32 v154, 3, v19
	v_bfe_u32 v155, v19, 2, 2
	v_bfe_u32 v156, v19, 4, 2
	v_bfe_u32 v157, v19, 6, 2
	s_mov_b32 s16, 0xfff0fff0
	s_movk_i32 s17, 0x3ffc
	v_pk_fma_f32 v[80:81], v[116:117], v[20:21], v[16:17] op_sel_hi:[1,0,0]
	v_pk_fma_f32 v[80:81], v[118:119], v[36:37], v[80:81] op_sel_hi:[1,0,1]
	s_nop 0
	v_exp_f32_e32 v82, v80
	v_exp_f32_e32 v83, v81
	s_nop 0
	v_cvt_pknorm_u16_f32 v158, v82, v83
	v_and_b32_e32 v159, s16, v158
	v_lshrrev_b32_sdwa v160, v165, v159 dst_sel:DWORD dst_unused:UNUSED_PAD src0_sel:DWORD src1_sel:WORD_0
	v_lshrrev_b32_sdwa v161, v165, v159 dst_sel:DWORD dst_unused:UNUSED_PAD src0_sel:DWORD src1_sel:WORD_1
	v_xor_b32_e32 v162, s17, v160
	v_xor_b32_e32 v163, s17, v161
	v_cmp_ne_u32_e32 vcc, 1, v154
	s_mov_b64 exec, vcc
	ds_add_u32 v160, v164 offset:1648
	s_not_b64 exec, vcc
	ds_add_u32 v162, v15 offset:1648
	v_mov_b32_e32 v150, v82
	s_mov_b64 exec, -1
	v_cmp_ne_u32_e32 vcc, 1, v155
	s_mov_b64 exec, vcc
	ds_add_u32 v161, v164 offset:1648
	s_not_b64 exec, vcc
	ds_add_u32 v163, v15 offset:1648
	v_mov_b32_e32 v151, v83
	s_mov_b64 exec, -1
	v_pk_fma_f32 v[80:81], v[116:117], v[20:21], v[16:17] op_sel:[0,1,1]
	v_pk_fma_f32 v[80:81], v[118:119], v[36:37], v[80:81] op_sel:[0,1,0]
	s_nop 0
	v_exp_f32_e32 v82, v80
	v_exp_f32_e32 v83, v81
	s_nop 0
	v_cvt_pknorm_u16_f32 v158, v82, v83
	v_and_b32_e32 v159, s16, v158
	v_lshrrev_b32_sdwa v160, v165, v159 dst_sel:DWORD dst_unused:UNUSED_PAD src0_sel:DWORD src1_sel:WORD_0
	v_lshrrev_b32_sdwa v161, v165, v159 dst_sel:DWORD dst_unused:UNUSED_PAD src0_sel:DWORD src1_sel:WORD_1
	v_xor_b32_e32 v162, s17, v160
	v_xor_b32_e32 v163, s17, v161
	v_cmp_ne_u32_e32 vcc, 2, v154
	s_mov_b64 exec, vcc
	ds_add_u32 v160, v164 offset:18032
	s_not_b64 exec, vcc
	ds_add_u32 v162, v15 offset:18032
	v_mov_b32_e32 v150, v82
	s_mov_b64 exec, -1
	v_cmp_ne_u32_e32 vcc, 2, v155
	s_mov_b64 exec, vcc
	ds_add_u32 v161, v164 offset:18032
	s_not_b64 exec, vcc
	ds_add_u32 v163, v15 offset:18032
	v_mov_b32_e32 v151, v83
	s_mov_b64 exec, -1
	v_pk_fma_f32 v[80:81], v[116:117], v[8:9], v[12:13] op_sel_hi:[1,0,0]
	v_pk_fma_f32 v[80:81], v[118:119], v[24:25], v[80:81] op_sel_hi:[1,0,1]
	s_nop 0
	v_exp_f32_e32 v82, v80
	v_exp_f32_e32 v83, v81
	s_nop 0
	v_cvt_pknorm_u16_f32 v158, v82, v83
	v_and_b32_e32 v159, s16, v158
	v_lshrrev_b32_sdwa v160, v165, v159 dst_sel:DWORD dst_unused:UNUSED_PAD src0_sel:DWORD src1_sel:WORD_0
	v_lshrrev_b32_sdwa v161, v165, v159 dst_sel:DWORD dst_unused:UNUSED_PAD src0_sel:DWORD src1_sel:WORD_1
	v_xor_b32_e32 v162, s17, v160
	v_xor_b32_e32 v163, s17, v161
	v_cmp_ne_u32_e32 vcc, 3, v154
	s_mov_b64 exec, vcc
	ds_add_u32 v160, v164 offset:34416
	s_not_b64 exec, vcc
	ds_add_u32 v162, v15 offset:34416
	v_mov_b32_e32 v150, v82
	s_mov_b64 exec, -1
	v_cmp_ne_u32_e32 vcc, 3, v155
	s_mov_b64 exec, vcc
	ds_add_u32 v161, v164 offset:34416
	s_not_b64 exec, vcc
	ds_add_u32 v163, v15 offset:34416
	v_mov_b32_e32 v151, v83
	s_mov_b64 exec, -1
	s_waitcnt lgkmcnt(12)
	v_pk_add_f32 v[166:167], v[76:77], v[150:151] neg_lo:[0,1] neg_hi:[0,1]
	s_nop 0
	v_pk_fma_f32 v[166:167], v[166:167], v[166:167], v[6:7]
	v_pk_fma_f32 v[80:81], v[120:121], v[20:21], v[16:17] op_sel_hi:[1,0,0]
	v_pk_fma_f32 v[80:81], v[122:123], v[36:37], v[80:81] op_sel_hi:[1,0,1]
	s_nop 0
	v_exp_f32_e32 v82, v80
	v_exp_f32_e32 v83, v81
	s_nop 0
	v_cvt_pknorm_u16_f32 v158, v82, v83
	v_and_b32_e32 v159, s16, v158
	v_lshrrev_b32_sdwa v160, v165, v159 dst_sel:DWORD dst_unused:UNUSED_PAD src0_sel:DWORD src1_sel:WORD_0
	v_lshrrev_b32_sdwa v161, v165, v159 dst_sel:DWORD dst_unused:UNUSED_PAD src0_sel:DWORD src1_sel:WORD_1
	v_xor_b32_e32 v162, s17, v160
	v_xor_b32_e32 v163, s17, v161
	v_cmp_ne_u32_e32 vcc, 1, v156
	s_mov_b64 exec, vcc
	ds_add_u32 v160, v164 offset:1648
	s_not_b64 exec, vcc
	ds_add_u32 v162, v15 offset:1648
	v_mov_b32_e32 v152, v82
	s_mov_b64 exec, -1
	v_cmp_ne_u32_e32 vcc, 1, v157
	s_mov_b64 exec, vcc
	ds_add_u32 v161, v164 offset:1648
	s_not_b64 exec, vcc
	ds_add_u32 v163, v15 offset:1648
	v_mov_b32_e32 v153, v83
	s_mov_b64 exec, -1
	v_pk_fma_f32 v[80:81], v[120:121], v[20:21], v[16:17] op_sel:[0,1,1]
	v_pk_fma_f32 v[80:81], v[122:123], v[36:37], v[80:81] op_sel:[0,1,0]
	s_nop 0
	v_exp_f32_e32 v82, v80
	v_exp_f32_e32 v83, v81
	s_nop 0
	v_cvt_pknorm_u16_f32 v158, v82, v83
	v_and_b32_e32 v159, s16, v158
	v_lshrrev_b32_sdwa v160, v165, v159 dst_sel:DWORD dst_unused:UNUSED_PAD src0_sel:DWORD src1_sel:WORD_0
	v_lshrrev_b32_sdwa v161, v165, v159 dst_sel:DWORD dst_unused:UNUSED_PAD src0_sel:DWORD src1_sel:WORD_1
	v_xor_b32_e32 v162, s17, v160
	v_xor_b32_e32 v163, s17, v161
	v_cmp_ne_u32_e32 vcc, 2, v156
	s_mov_b64 exec, vcc
	ds_add_u32 v160, v164 offset:18032
	s_not_b64 exec, vcc
	ds_add_u32 v162, v15 offset:18032
	v_mov_b32_e32 v152, v82
	s_mov_b64 exec, -1
	v_cmp_ne_u32_e32 vcc, 2, v157
	s_mov_b64 exec, vcc
	ds_add_u32 v161, v164 offset:18032
	s_not_b64 exec, vcc
	ds_add_u32 v163, v15 offset:18032
	v_mov_b32_e32 v153, v83
	s_mov_b64 exec, -1
	v_pk_fma_f32 v[80:81], v[120:121], v[8:9], v[12:13] op_sel_hi:[1,0,0]
	v_pk_fma_f32 v[80:81], v[122:123], v[24:25], v[80:81] op_sel_hi:[1,0,1]
	s_nop 0
	v_exp_f32_e32 v82, v80
	v_exp_f32_e32 v83, v81
	s_nop 0
	v_cvt_pknorm_u16_f32 v158, v82, v83
	v_and_b32_e32 v159, s16, v158
	v_lshrrev_b32_sdwa v160, v165, v159 dst_sel:DWORD dst_unused:UNUSED_PAD src0_sel:DWORD src1_sel:WORD_0
	v_lshrrev_b32_sdwa v161, v165, v159 dst_sel:DWORD dst_unused:UNUSED_PAD src0_sel:DWORD src1_sel:WORD_1
	v_xor_b32_e32 v162, s17, v160
	v_xor_b32_e32 v163, s17, v161
	v_cmp_ne_u32_e32 vcc, 3, v156
	s_mov_b64 exec, vcc
	ds_add_u32 v160, v164 offset:34416
	s_not_b64 exec, vcc
	ds_add_u32 v162, v15 offset:34416
	v_mov_b32_e32 v152, v82
	s_mov_b64 exec, -1
	v_cmp_ne_u32_e32 vcc, 3, v157
	s_mov_b64 exec, vcc
	ds_add_u32 v161, v164 offset:34416
	s_not_b64 exec, vcc
	ds_add_u32 v163, v15 offset:34416
	v_mov_b32_e32 v153, v83
	s_mov_b64 exec, -1
	v_pk_add_f32 v[80:81], v[78:79], v[152:153] neg_lo:[0,1] neg_hi:[0,1]
	s_nop 0
	v_pk_fma_f32 v[6:7], v[80:81], v[80:81], v[166:167]
	ds_read_b128 v[76:79], v135
	v_mov_b32_e32 v164, 1
	v_mov_b32_e32 v165, 2
	v_mov_b32_e32 v150, 0
	v_mov_b32_e32 v151, 0
	v_mov_b32_e32 v152, 0
	v_mov_b32_e32 v153, 0
	v_and_b32_e32 v154, 3, v13
	v_bfe_u32 v155, v13, 2, 2
	v_bfe_u32 v156, v13, 4, 2
	v_bfe_u32 v157, v13, 6, 2
	s_mov_b32 s16, 0xfff0fff0
	s_movk_i32 s17, 0x3ffc
	v_pk_fma_f32 v[80:81], v[58:59], v[20:21], v[16:17] op_sel_hi:[1,0,0]
	v_pk_fma_f32 v[80:81], v[124:125], v[36:37], v[80:81] op_sel_hi:[1,0,1]
	s_nop 0
	v_exp_f32_e32 v82, v80
	v_exp_f32_e32 v83, v81
	s_nop 0
	v_cvt_pknorm_u16_f32 v158, v82, v83
	v_and_b32_e32 v159, s16, v158
	v_lshrrev_b32_sdwa v160, v165, v159 dst_sel:DWORD dst_unused:UNUSED_PAD src0_sel:DWORD src1_sel:WORD_0
	v_lshrrev_b32_sdwa v161, v165, v159 dst_sel:DWORD dst_unused:UNUSED_PAD src0_sel:DWORD src1_sel:WORD_1
	v_xor_b32_e32 v162, s17, v160
	v_xor_b32_e32 v163, s17, v161
	v_cmp_ne_u32_e32 vcc, 1, v154
	s_mov_b64 exec, vcc
	ds_add_u32 v160, v164 offset:1648
	s_not_b64 exec, vcc
	ds_add_u32 v162, v15 offset:1648
	v_mov_b32_e32 v150, v82
	s_mov_b64 exec, -1
	v_cmp_ne_u32_e32 vcc, 1, v155
	s_mov_b64 exec, vcc
	ds_add_u32 v161, v164 offset:1648
	s_not_b64 exec, vcc
	ds_add_u32 v163, v15 offset:1648
	v_mov_b32_e32 v151, v83
	s_mov_b64 exec, -1
	v_pk_fma_f32 v[80:81], v[58:59], v[20:21], v[16:17] op_sel:[0,1,1]
	v_pk_fma_f32 v[80:81], v[124:125], v[36:37], v[80:81] op_sel:[0,1,0]
	s_nop 0
	v_exp_f32_e32 v82, v80
	v_exp_f32_e32 v83, v81
	s_nop 0
	v_cvt_pknorm_u16_f32 v158, v82, v83
	v_and_b32_e32 v159, s16, v158
	v_lshrrev_b32_sdwa v160, v165, v159 dst_sel:DWORD dst_unused:UNUSED_PAD src0_sel:DWORD src1_sel:WORD_0
	v_lshrrev_b32_sdwa v161, v165, v159 dst_sel:DWORD dst_unused:UNUSED_PAD src0_sel:DWORD src1_sel:WORD_1
	v_xor_b32_e32 v162, s17, v160
	v_xor_b32_e32 v163, s17, v161
	v_cmp_ne_u32_e32 vcc, 2, v154
	s_mov_b64 exec, vcc
	ds_add_u32 v160, v164 offset:18032
	s_not_b64 exec, vcc
	ds_add_u32 v162, v15 offset:18032
	v_mov_b32_e32 v150, v82
	s_mov_b64 exec, -1
	v_cmp_ne_u32_e32 vcc, 2, v155
	s_mov_b64 exec, vcc
	ds_add_u32 v161, v164 offset:18032
	s_not_b64 exec, vcc
	ds_add_u32 v163, v15 offset:18032
	v_mov_b32_e32 v151, v83
	s_mov_b64 exec, -1
	v_pk_fma_f32 v[80:81], v[58:59], v[8:9], v[12:13] op_sel_hi:[1,0,0]
	v_pk_fma_f32 v[80:81], v[124:125], v[24:25], v[80:81] op_sel_hi:[1,0,1]
	s_nop 0
	v_exp_f32_e32 v82, v80
	v_exp_f32_e32 v83, v81
	s_nop 0
	v_cvt_pknorm_u16_f32 v158, v82, v83
	v_and_b32_e32 v159, s16, v158
	v_lshrrev_b32_sdwa v160, v165, v159 dst_sel:DWORD dst_unused:UNUSED_PAD src0_sel:DWORD src1_sel:WORD_0
	v_lshrrev_b32_sdwa v161, v165, v159 dst_sel:DWORD dst_unused:UNUSED_PAD src0_sel:DWORD src1_sel:WORD_1
	v_xor_b32_e32 v162, s17, v160
	v_xor_b32_e32 v163, s17, v161
	v_cmp_ne_u32_e32 vcc, 3, v154
	s_mov_b64 exec, vcc
	ds_add_u32 v160, v164 offset:34416
	s_not_b64 exec, vcc
	ds_add_u32 v162, v15 offset:34416
	v_mov_b32_e32 v150, v82
	s_mov_b64 exec, -1
	v_cmp_ne_u32_e32 vcc, 3, v155
	s_mov_b64 exec, vcc
	ds_add_u32 v161, v164 offset:34416
	s_not_b64 exec, vcc
	ds_add_u32 v163, v15 offset:34416
	v_mov_b32_e32 v151, v83
	s_mov_b64 exec, -1
	s_waitcnt lgkmcnt(12)
	v_pk_add_f32 v[166:167], v[76:77], v[150:151] neg_lo:[0,1] neg_hi:[0,1]
	s_nop 0
	v_pk_fma_f32 v[166:167], v[166:167], v[166:167], v[6:7]
	v_pk_fma_f32 v[80:81], v[60:61], v[20:21], v[16:17] op_sel_hi:[1,0,0]
	v_pk_fma_f32 v[80:81], v[126:127], v[36:37], v[80:81] op_sel_hi:[1,0,1]
	s_nop 0
	v_exp_f32_e32 v82, v80
	v_exp_f32_e32 v83, v81
	s_nop 0
	v_cvt_pknorm_u16_f32 v158, v82, v83
	v_and_b32_e32 v159, s16, v158
	v_lshrrev_b32_sdwa v160, v165, v159 dst_sel:DWORD dst_unused:UNUSED_PAD src0_sel:DWORD src1_sel:WORD_0
	v_lshrrev_b32_sdwa v161, v165, v159 dst_sel:DWORD dst_unused:UNUSED_PAD src0_sel:DWORD src1_sel:WORD_1
	v_xor_b32_e32 v162, s17, v160
	v_xor_b32_e32 v163, s17, v161
	v_cmp_ne_u32_e32 vcc, 1, v156
	s_mov_b64 exec, vcc
	ds_add_u32 v160, v164 offset:1648
	s_not_b64 exec, vcc
	ds_add_u32 v162, v15 offset:1648
	v_mov_b32_e32 v152, v82
	s_mov_b64 exec, -1
	v_cmp_ne_u32_e32 vcc, 1, v157
	s_mov_b64 exec, vcc
	ds_add_u32 v161, v164 offset:1648
	s_not_b64 exec, vcc
	ds_add_u32 v163, v15 offset:1648
	v_mov_b32_e32 v153, v83
	s_mov_b64 exec, -1
	v_pk_fma_f32 v[80:81], v[60:61], v[20:21], v[16:17] op_sel:[0,1,1]
	v_pk_fma_f32 v[80:81], v[126:127], v[36:37], v[80:81] op_sel:[0,1,0]
	s_nop 0
	v_exp_f32_e32 v82, v80
	v_exp_f32_e32 v83, v81
	s_nop 0
	v_cvt_pknorm_u16_f32 v158, v82, v83
	v_and_b32_e32 v159, s16, v158
	v_lshrrev_b32_sdwa v160, v165, v159 dst_sel:DWORD dst_unused:UNUSED_PAD src0_sel:DWORD src1_sel:WORD_0
	v_lshrrev_b32_sdwa v161, v165, v159 dst_sel:DWORD dst_unused:UNUSED_PAD src0_sel:DWORD src1_sel:WORD_1
	v_xor_b32_e32 v162, s17, v160
	v_xor_b32_e32 v163, s17, v161
	v_cmp_ne_u32_e32 vcc, 2, v156
	s_mov_b64 exec, vcc
	ds_add_u32 v160, v164 offset:18032
	s_not_b64 exec, vcc
	ds_add_u32 v162, v15 offset:18032
	v_mov_b32_e32 v152, v82
	s_mov_b64 exec, -1
	v_cmp_ne_u32_e32 vcc, 2, v157
	s_mov_b64 exec, vcc
	ds_add_u32 v161, v164 offset:18032
	s_not_b64 exec, vcc
	ds_add_u32 v163, v15 offset:18032
	v_mov_b32_e32 v153, v83
	s_mov_b64 exec, -1
	v_pk_fma_f32 v[80:81], v[60:61], v[8:9], v[12:13] op_sel_hi:[1,0,0]
	v_pk_fma_f32 v[80:81], v[126:127], v[24:25], v[80:81] op_sel_hi:[1,0,1]
	s_nop 0
	v_exp_f32_e32 v82, v80
	v_exp_f32_e32 v83, v81
	s_nop 0
	v_cvt_pknorm_u16_f32 v158, v82, v83
	v_and_b32_e32 v159, s16, v158
	v_lshrrev_b32_sdwa v160, v165, v159 dst_sel:DWORD dst_unused:UNUSED_PAD src0_sel:DWORD src1_sel:WORD_0
	v_lshrrev_b32_sdwa v161, v165, v159 dst_sel:DWORD dst_unused:UNUSED_PAD src0_sel:DWORD src1_sel:WORD_1
	v_xor_b32_e32 v162, s17, v160
	v_xor_b32_e32 v163, s17, v161
	v_cmp_ne_u32_e32 vcc, 3, v156
	s_mov_b64 exec, vcc
	ds_add_u32 v160, v164 offset:34416
	s_not_b64 exec, vcc
	ds_add_u32 v162, v15 offset:34416
	v_mov_b32_e32 v152, v82
	s_mov_b64 exec, -1
	v_cmp_ne_u32_e32 vcc, 3, v157
	s_mov_b64 exec, vcc
	ds_add_u32 v161, v164 offset:34416
	s_not_b64 exec, vcc
	ds_add_u32 v163, v15 offset:34416
	v_mov_b32_e32 v153, v83
	s_mov_b64 exec, -1
	v_pk_add_f32 v[80:81], v[78:79], v[152:153] neg_lo:[0,1] neg_hi:[0,1]
	s_nop 0
	v_pk_fma_f32 v[6:7], v[80:81], v[80:81], v[166:167]
	ds_read_b128 v[76:79], v70
	v_mov_b32_e32 v164, 1
	v_mov_b32_e32 v165, 2
	v_mov_b32_e32 v150, 0
	v_mov_b32_e32 v151, 0
	v_mov_b32_e32 v152, 0
	v_mov_b32_e32 v153, 0
	v_and_b32_e32 v154, 3, v9
	v_bfe_u32 v155, v9, 2, 2
	v_bfe_u32 v156, v9, 4, 2
	v_bfe_u32 v157, v9, 6, 2
	s_mov_b32 s16, 0xfff0fff0
	s_movk_i32 s17, 0x3ffc
	v_pk_fma_f32 v[80:81], v[62:63], v[20:21], v[16:17] op_sel_hi:[1,0,0]
	v_pk_fma_f32 v[80:81], v[66:67], v[36:37], v[80:81] op_sel_hi:[1,0,1]
	s_nop 0
	v_exp_f32_e32 v82, v80
	v_exp_f32_e32 v83, v81
	s_nop 0
	v_cvt_pknorm_u16_f32 v158, v82, v83
	v_and_b32_e32 v159, s16, v158
	v_lshrrev_b32_sdwa v160, v165, v159 dst_sel:DWORD dst_unused:UNUSED_PAD src0_sel:DWORD src1_sel:WORD_0
	v_lshrrev_b32_sdwa v161, v165, v159 dst_sel:DWORD dst_unused:UNUSED_PAD src0_sel:DWORD src1_sel:WORD_1
	v_xor_b32_e32 v162, s17, v160
	v_xor_b32_e32 v163, s17, v161
	v_cmp_ne_u32_e32 vcc, 1, v154
	s_mov_b64 exec, vcc
	ds_add_u32 v160, v164 offset:1648
	s_not_b64 exec, vcc
	ds_add_u32 v162, v15 offset:1648
	v_mov_b32_e32 v150, v82
	s_mov_b64 exec, -1
	v_cmp_ne_u32_e32 vcc, 1, v155
	s_mov_b64 exec, vcc
	ds_add_u32 v161, v164 offset:1648
	s_not_b64 exec, vcc
	ds_add_u32 v163, v15 offset:1648
	v_mov_b32_e32 v151, v83
	s_mov_b64 exec, -1
	v_pk_fma_f32 v[80:81], v[62:63], v[20:21], v[16:17] op_sel:[0,1,1]
	v_pk_fma_f32 v[80:81], v[66:67], v[36:37], v[80:81] op_sel:[0,1,0]
	s_nop 0
	v_exp_f32_e32 v82, v80
	v_exp_f32_e32 v83, v81
	s_nop 0
	v_cvt_pknorm_u16_f32 v158, v82, v83
	v_and_b32_e32 v159, s16, v158
	v_lshrrev_b32_sdwa v160, v165, v159 dst_sel:DWORD dst_unused:UNUSED_PAD src0_sel:DWORD src1_sel:WORD_0
	v_lshrrev_b32_sdwa v161, v165, v159 dst_sel:DWORD dst_unused:UNUSED_PAD src0_sel:DWORD src1_sel:WORD_1
	v_xor_b32_e32 v162, s17, v160
	v_xor_b32_e32 v163, s17, v161
	v_cmp_ne_u32_e32 vcc, 2, v154
	s_mov_b64 exec, vcc
	ds_add_u32 v160, v164 offset:18032
	s_not_b64 exec, vcc
	ds_add_u32 v162, v15 offset:18032
	v_mov_b32_e32 v150, v82
	s_mov_b64 exec, -1
	v_cmp_ne_u32_e32 vcc, 2, v155
	s_mov_b64 exec, vcc
	ds_add_u32 v161, v164 offset:18032
	s_not_b64 exec, vcc
	ds_add_u32 v163, v15 offset:18032
	v_mov_b32_e32 v151, v83
	s_mov_b64 exec, -1
	v_pk_fma_f32 v[80:81], v[62:63], v[8:9], v[12:13] op_sel_hi:[1,0,0]
	v_pk_fma_f32 v[80:81], v[66:67], v[24:25], v[80:81] op_sel_hi:[1,0,1]
	s_nop 0
	v_exp_f32_e32 v82, v80
	v_exp_f32_e32 v83, v81
	s_nop 0
	v_cvt_pknorm_u16_f32 v158, v82, v83
	v_and_b32_e32 v159, s16, v158
	v_lshrrev_b32_sdwa v160, v165, v159 dst_sel:DWORD dst_unused:UNUSED_PAD src0_sel:DWORD src1_sel:WORD_0
	v_lshrrev_b32_sdwa v161, v165, v159 dst_sel:DWORD dst_unused:UNUSED_PAD src0_sel:DWORD src1_sel:WORD_1
	v_xor_b32_e32 v162, s17, v160
	v_xor_b32_e32 v163, s17, v161
	v_cmp_ne_u32_e32 vcc, 3, v154
	s_mov_b64 exec, vcc
	ds_add_u32 v160, v164 offset:34416
	s_not_b64 exec, vcc
	ds_add_u32 v162, v15 offset:34416
	v_mov_b32_e32 v150, v82
	s_mov_b64 exec, -1
	v_cmp_ne_u32_e32 vcc, 3, v155
	s_mov_b64 exec, vcc
	ds_add_u32 v161, v164 offset:34416
	s_not_b64 exec, vcc
	ds_add_u32 v163, v15 offset:34416
	v_mov_b32_e32 v151, v83
	s_mov_b64 exec, -1
	s_waitcnt lgkmcnt(12)
	v_pk_add_f32 v[166:167], v[76:77], v[150:151] neg_lo:[0,1] neg_hi:[0,1]
	s_nop 0
	v_pk_fma_f32 v[166:167], v[166:167], v[166:167], v[6:7]
	v_pk_fma_f32 v[80:81], v[64:65], v[20:21], v[16:17] op_sel_hi:[1,0,0]
	v_pk_fma_f32 v[80:81], v[68:69], v[36:37], v[80:81] op_sel_hi:[1,0,1]
	s_nop 0
	v_exp_f32_e32 v82, v80
	v_exp_f32_e32 v83, v81
	s_nop 0
	v_cvt_pknorm_u16_f32 v158, v82, v83
	v_and_b32_e32 v159, s16, v158
	v_lshrrev_b32_sdwa v160, v165, v159 dst_sel:DWORD dst_unused:UNUSED_PAD src0_sel:DWORD src1_sel:WORD_0
	v_lshrrev_b32_sdwa v161, v165, v159 dst_sel:DWORD dst_unused:UNUSED_PAD src0_sel:DWORD src1_sel:WORD_1
	v_xor_b32_e32 v162, s17, v160
	v_xor_b32_e32 v163, s17, v161
	v_cmp_ne_u32_e32 vcc, 1, v156
	s_mov_b64 exec, vcc
	ds_add_u32 v160, v164 offset:1648
	s_not_b64 exec, vcc
	ds_add_u32 v162, v15 offset:1648
	v_mov_b32_e32 v152, v82
	s_mov_b64 exec, -1
	v_cmp_ne_u32_e32 vcc, 1, v157
	s_mov_b64 exec, vcc
	ds_add_u32 v161, v164 offset:1648
	s_not_b64 exec, vcc
	ds_add_u32 v163, v15 offset:1648
	v_mov_b32_e32 v153, v83
	s_mov_b64 exec, -1
	v_pk_fma_f32 v[80:81], v[64:65], v[20:21], v[16:17] op_sel:[0,1,1]
	v_pk_fma_f32 v[80:81], v[68:69], v[36:37], v[80:81] op_sel:[0,1,0]
	s_nop 0
	v_exp_f32_e32 v82, v80
	v_exp_f32_e32 v83, v81
	s_nop 0
	v_cvt_pknorm_u16_f32 v158, v82, v83
	v_and_b32_e32 v159, s16, v158
	v_lshrrev_b32_sdwa v160, v165, v159 dst_sel:DWORD dst_unused:UNUSED_PAD src0_sel:DWORD src1_sel:WORD_0
	v_lshrrev_b32_sdwa v161, v165, v159 dst_sel:DWORD dst_unused:UNUSED_PAD src0_sel:DWORD src1_sel:WORD_1
	v_xor_b32_e32 v162, s17, v160
	v_xor_b32_e32 v163, s17, v161
	v_cmp_ne_u32_e32 vcc, 2, v156
	s_mov_b64 exec, vcc
	ds_add_u32 v160, v164 offset:18032
	s_not_b64 exec, vcc
	ds_add_u32 v162, v15 offset:18032
	v_mov_b32_e32 v152, v82
	s_mov_b64 exec, -1
	v_cmp_ne_u32_e32 vcc, 2, v157
	s_mov_b64 exec, vcc
	ds_add_u32 v161, v164 offset:18032
	s_not_b64 exec, vcc
	ds_add_u32 v163, v15 offset:18032
	v_mov_b32_e32 v153, v83
	s_mov_b64 exec, -1
	v_pk_fma_f32 v[80:81], v[64:65], v[8:9], v[12:13] op_sel_hi:[1,0,0]
	v_pk_fma_f32 v[80:81], v[68:69], v[24:25], v[80:81] op_sel_hi:[1,0,1]
	s_nop 0
	v_exp_f32_e32 v82, v80
	v_exp_f32_e32 v83, v81
	s_nop 0
	v_cvt_pknorm_u16_f32 v158, v82, v83
	v_and_b32_e32 v159, s16, v158
	v_lshrrev_b32_sdwa v160, v165, v159 dst_sel:DWORD dst_unused:UNUSED_PAD src0_sel:DWORD src1_sel:WORD_0
	v_lshrrev_b32_sdwa v161, v165, v159 dst_sel:DWORD dst_unused:UNUSED_PAD src0_sel:DWORD src1_sel:WORD_1
	v_xor_b32_e32 v162, s17, v160
	v_xor_b32_e32 v163, s17, v161
	v_cmp_ne_u32_e32 vcc, 3, v156
	s_mov_b64 exec, vcc
	ds_add_u32 v160, v164 offset:34416
	s_not_b64 exec, vcc
	ds_add_u32 v162, v15 offset:34416
	v_mov_b32_e32 v152, v82
	s_mov_b64 exec, -1
	v_cmp_ne_u32_e32 vcc, 3, v157
	s_mov_b64 exec, vcc
	ds_add_u32 v161, v164 offset:34416
	s_not_b64 exec, vcc
	ds_add_u32 v163, v15 offset:34416
	v_mov_b32_e32 v153, v83
	s_mov_b64 exec, -1
	v_pk_add_f32 v[80:81], v[78:79], v[152:153] neg_lo:[0,1] neg_hi:[0,1]
	s_nop 0
	v_pk_fma_f32 v[6:7], v[80:81], v[80:81], v[166:167]
	s_and_saveexec_b64 s[8:9], s[4:5]
	s_cbranch_execz .LBB0_60
	v_mov_b32_e32 v22, v20
	v_mov_b32_e32 v23, v20
	v_mov_b32_e32 v24, v16
	v_mov_b32_e32 v25, v16
	v_mov_b32_e32 v18, v36
	v_mov_b32_e32 v19, v36
	v_pk_fma_f32 v[2:3], v[54:55], v[22:23], v[24:25]
	v_add_u32_e32 v1, 0x18000, v1
	v_pk_fma_f32 v[2:3], v[50:51], v[18:19], v[2:3]
	v_bfe_u32 v30, v40, 2, 2
	v_exp_f32_e32 v10, v2
	v_exp_f32_e32 v14, v3
	ds_read_b128 v[2:5], v1
	v_and_b32_e32 v1, 3, v40
	v_cmp_eq_u32_e32 vcc, 1, v1
	v_cvt_pknorm_u16_f32 v28, v10, v14
	v_lshrrev_b32_e32 v29, 4, v28
	v_bfe_u32 v31, v28, 4, 12
	v_bitop3_b32 v29, v29, s3, v29 bitop3:0xc
	v_cndmask_b32_e32 v29, v31, v29, vcc
	v_lshl_add_u32 v29, v29, 2, v11
	v_cndmask_b32_e32 v31, 1, v15, vcc
	v_lshrrev_b32_e32 v28, 20, v28
	ds_add_u32 v29, v31
	v_cndmask_b32_e32 v10, 0, v10, vcc
	v_xor_b32_e32 v29, 0xfff, v28
	v_cmp_eq_u32_e32 vcc, 1, v30
	v_mov_b32_e32 v20, v21
	v_mov_b32_e32 v16, v17
	v_cndmask_b32_e32 v28, v28, v29, vcc
	v_mov_b32_e32 v36, v37
	v_lshl_add_u32 v31, v28, 2, v11
	v_pk_fma_f32 v[28:29], v[54:55], v[20:21], v[16:17]
	v_cndmask_b32_e32 v14, 0, v14, vcc
	v_pk_fma_f32 v[28:29], v[50:51], v[36:37], v[28:29]
	v_mov_b32_e32 v9, v8
	v_exp_f32_e32 v28, v28
	v_exp_f32_e32 v32, v29
	v_cndmask_b32_e32 v29, 1, v15, vcc
	ds_add_u32 v31, v29
	v_cmp_eq_u32_e32 vcc, 2, v1
	v_cvt_pknorm_u16_f32 v29, v28, v32
	v_lshrrev_b32_e32 v31, 4, v29
	v_bfe_u32 v33, v29, 4, 12
	v_bitop3_b32 v31, v31, s3, v31 bitop3:0xc
	v_cndmask_b32_e32 v10, v10, v28, vcc
	v_lshrrev_b32_e32 v28, 20, v29
	v_cndmask_b32_e32 v31, v33, v31, vcc
	v_cndmask_b32_e32 v33, 1, v15, vcc
	v_xor_b32_e32 v29, 0xfff, v28
	v_cmp_eq_u32_e32 vcc, 2, v30
	v_mov_b32_e32 v13, v12
	v_lshl_add_u32 v31, v31, 2, v11
	v_cndmask_b32_e32 v28, v28, v29, vcc
	v_mov_b32_e32 v26, v38
	v_mov_b32_e32 v27, v38
	ds_add_u32 v31, v33 offset:16384
	v_lshl_add_u32 v31, v28, 2, v11
	v_pk_fma_f32 v[28:29], v[54:55], v[8:9], v[12:13]
	v_cndmask_b32_e32 v33, 1, v15, vcc
	v_pk_fma_f32 v[28:29], v[50:51], v[26:27], v[28:29]
	ds_add_u32 v31, v33 offset:16384
	v_exp_f32_e32 v28, v28
	v_exp_f32_e32 v29, v29
	v_cndmask_b32_e32 v14, v14, v32, vcc
	v_cmp_eq_u32_e32 vcc, 3, v1
	v_pk_fma_f32 v[22:23], v[22:23], v[46:47], v[24:25]
	v_cvt_pknorm_u16_f32 v31, v28, v29
	v_lshrrev_b32_e32 v32, 4, v31
	v_bfe_u32 v33, v31, 4, 12
	v_bitop3_b32 v32, v32, s3, v32 bitop3:0xc
	v_cndmask_b32_e32 v1, v33, v32, vcc
	v_lshl_add_u32 v1, v1, 2, v11
	v_cndmask_b32_e32 v32, 1, v15, vcc
	ds_add_u32 v1, v32 offset:32768
	v_lshrrev_b32_e32 v1, 20, v31
	v_cndmask_b32_e32 v28, v10, v28, vcc
	v_xor_b32_e32 v10, 0xfff, v1
	v_cmp_eq_u32_e32 vcc, 3, v30
	v_pk_fma_f32 v[18:19], v[18:19], v[74:75], v[22:23]
	s_nop 0
	v_cndmask_b32_e32 v1, v1, v10, vcc
	v_lshl_add_u32 v1, v1, 2, v11
	v_cndmask_b32_e32 v10, 1, v15, vcc
	ds_add_u32 v1, v10 offset:32768
	v_exp_f32_e32 v1, v18
	v_exp_f32_e32 v10, v19
	v_cndmask_b32_e32 v29, v14, v29, vcc
	s_waitcnt lgkmcnt(6)
	v_pk_add_f32 v[2:3], v[2:3], v[28:29] neg_lo:[0,1] neg_hi:[0,1]
	v_bfe_u32 v14, v40, 4, 2
	v_pk_fma_f32 v[2:3], v[2:3], v[2:3], v[6:7]
	v_cvt_pknorm_u16_f32 v6, v1, v10
	v_lshrrev_b32_e32 v7, 4, v6
	v_bfe_u32 v19, v6, 4, 12
	v_bitop3_b32 v7, v7, s3, v7 bitop3:0xc
	v_cmp_eq_u32_e32 vcc, 1, v14
	v_bfe_u32 v18, v40, 6, 2
	v_lshrrev_b32_e32 v6, 20, v6
	v_cndmask_b32_e32 v7, v19, v7, vcc
	v_lshl_add_u32 v7, v7, 2, v11
	v_cndmask_b32_e32 v19, 1, v15, vcc
	ds_add_u32 v7, v19
	v_cndmask_b32_e32 v1, 0, v1, vcc
	v_xor_b32_e32 v7, 0xfff, v6
	v_cmp_eq_u32_e32 vcc, 1, v18
	v_cmp_eq_u32_e64 s[4:5], 3, v18
	s_nop 0
	v_cndmask_b32_e32 v6, v6, v7, vcc
	v_lshl_add_u32 v19, v6, 2, v11
	v_pk_fma_f32 v[6:7], v[20:21], v[46:47], v[16:17]
	v_cndmask_b32_e32 v10, 0, v10, vcc
	v_pk_fma_f32 v[6:7], v[36:37], v[74:75], v[6:7]
	s_nop 0
	v_exp_f32_e32 v6, v6
	v_exp_f32_e32 v16, v7
	v_cndmask_b32_e32 v7, 1, v15, vcc
	ds_add_u32 v19, v7
	v_cmp_eq_u32_e32 vcc, 2, v14
	v_cvt_pknorm_u16_f32 v7, v6, v16
	v_lshrrev_b32_e32 v17, 4, v7
	v_bfe_u32 v19, v7, 4, 12
	v_bitop3_b32 v17, v17, s3, v17 bitop3:0xc
	v_cndmask_b32_e32 v1, v1, v6, vcc
	v_lshrrev_b32_e32 v6, 20, v7
	v_cndmask_b32_e32 v17, v19, v17, vcc
	v_cndmask_b32_e32 v19, 1, v15, vcc
	v_xor_b32_e32 v7, 0xfff, v6
	v_cmp_eq_u32_e32 vcc, 2, v18
	v_lshl_add_u32 v17, v17, 2, v11
	ds_add_u32 v17, v19 offset:16384
	v_cndmask_b32_e32 v6, v6, v7, vcc
	v_lshl_add_u32 v17, v6, 2, v11
	v_pk_fma_f32 v[6:7], v[8:9], v[46:47], v[12:13]
	v_cndmask_b32_e32 v8, 1, v15, vcc
	v_pk_fma_f32 v[6:7], v[26:27], v[74:75], v[6:7]
	ds_add_u32 v17, v8 offset:16384
	v_exp_f32_e32 v6, v6
	v_exp_f32_e32 v7, v7
	v_cndmask_b32_e32 v8, v10, v16, vcc
	v_cmp_eq_u32_e32 vcc, 3, v14
	v_cvt_pknorm_u16_f32 v9, v6, v7
	v_lshrrev_b32_e32 v10, 4, v9
	v_bfe_u32 v12, v9, 4, 12
	v_bitop3_b32 v10, v10, s3, v10 bitop3:0xc
	v_cndmask_b32_e32 v10, v12, v10, vcc
	v_lshl_add_u32 v10, v10, 2, v11
	v_cndmask_b32_e32 v12, 1, v15, vcc
	v_lshrrev_b32_e32 v9, 20, v9
	ds_add_u32 v10, v12 offset:32768
	v_xor_b32_e32 v10, 0xfff, v9
	v_cndmask_b32_e64 v9, v9, v10, s[4:5]
	v_lshl_add_u32 v9, v9, 2, v11
	v_cndmask_b32_e64 v10, 1, v15, s[4:5]
	ds_add_u32 v9, v10 offset:32768
	v_cndmask_b32_e32 v6, v1, v6, vcc
	v_cndmask_b32_e64 v7, v8, v7, s[4:5]
	v_pk_add_f32 v[4:5], v[4:5], v[6:7] neg_lo:[0,1] neg_hi:[0,1]
	s_nop 0
	v_pk_fma_f32 v[6:7], v[4:5], v[4:5], v[2:3]

	.amdhsa_kernel _Z7kf_mainPKfPKiPfPjS3_S4_
		.amdhsa_group_segment_fixed_size 1648
		.amdhsa_private_segment_fixed_size 0
		.amdhsa_kernarg_size 48
		.amdhsa_user_sgpr_count 2
		.amdhsa_user_sgpr_dispatch_ptr 0
		.amdhsa_user_sgpr_queue_ptr 0
		.amdhsa_user_sgpr_kernarg_segment_ptr 1
		.amdhsa_user_sgpr_dispatch_id 0
		.amdhsa_user_sgpr_kernarg_preload_length 0
		.amdhsa_user_sgpr_kernarg_preload_offset 0
		.amdhsa_user_sgpr_private_segment_size 0
		.amdhsa_uses_dynamic_stack 0
		.amdhsa_enable_private_segment 0
		.amdhsa_system_sgpr_workgroup_id_x 1
		.amdhsa_system_sgpr_workgroup_id_y 0
		.amdhsa_system_sgpr_workgroup_id_z 0
		.amdhsa_system_sgpr_workgroup_info 0
		.amdhsa_system_vgpr_workitem_id 0
		.amdhsa_next_free_vgpr 168
		.amdhsa_next_free_sgpr 25
		.amdhsa_accum_offset 168
		.amdhsa_reserve_vcc 1
		.amdhsa_float_round_mode_32 0
		.amdhsa_float_round_mode_16_64 0
		.amdhsa_float_denorm_mode_32 3
		.amdhsa_float_denorm_mode_16_64 3
		.amdhsa_dx10_clamp 1
		.amdhsa_ieee_mode 1
		.amdhsa_fp16_overflow 0
		.amdhsa_tg_split 0
		.amdhsa_exception_fp_ieee_invalid_op 0
		.amdhsa_exception_fp_denorm_src 0
		.amdhsa_exception_fp_ieee_div_zero 0
		.amdhsa_exception_fp_ieee_overflow 0
		.amdhsa_exception_fp_ieee_underflow 0
		.amdhsa_exception_fp_ieee_inexact 0
		.amdhsa_exception_int_div_zero 0
	.end_amdhsa_kernel

amdhsa.kernels:
  - .agpr_count:     0
    .args:
      - .actual_access:  read_only
        .address_space:  global
        .offset:         0
        .size:           8
        .value_kind:     global_buffer
      - .actual_access:  read_only
        .address_space:  global
        .offset:         8
        .size:           8
        .value_kind:     global_buffer
      - .address_space:  global
        .offset:         16
        .size:           8
        .value_kind:     global_buffer
      - .actual_access:  write_only
        .address_space:  global
        .offset:         24
        .size:           8
        .value_kind:     global_buffer
      - .actual_access:  write_only
        .address_space:  global
        .offset:         32
        .size:           8
        .value_kind:     global_buffer
      - .address_space:  global
        .offset:         40
        .size:           8
        .value_kind:     global_buffer
    .group_segment_fixed_size: 1648
    .kernarg_segment_align: 8
    .kernarg_segment_size: 48
    .language:       OpenCL C
    .language_version:
      - 2
      - 0
    .max_flat_workgroup_size: 768
    .name:           _Z7kf_mainPKfPKiPfPjS3_S4_
    .private_segment_fixed_size: 0
    .sgpr_count:     31
    .sgpr_spill_count: 0
    .symbol:         _Z7kf_mainPKfPKiPfPjS3_S4_.kd
    .uniform_work_group_size: 1
    .uses_dynamic_stack: false
    .vgpr_count:     168
    .vgpr_spill_count: 0
    .wavefront_size: 64
  - .agpr_count:     0
    .args:
      - .actual_access:  read_only
        .address_space:  global
        .offset:         0
        .size:           8
        .value_kind:     global_buffer
      - .actual_access:  read_only
        .address_space:  global
        .offset:         8
        .size:           8
        .value_kind:     global_buffer
      - .actual_access:  write_only
        .address_space:  global
        .offset:         16
        .size:           8
        .value_kind:     global_buffer
    .group_segment_fixed_size: 192
    .kernarg_segment_align: 8
    .kernarg_segment_size: 24
    .language:       OpenCL C
    .language_version:
      - 2
      - 0
    .max_flat_workgroup_size: 256
    .name:           _Z8k1_statsPKfPKiPf
    .private_segment_fixed_size: 0
    .sgpr_count:     48
    .sgpr_spill_count: 0
    .symbol:         _Z8k1_statsPKfPKiPf.kd
    .uniform_work_group_size: 1
    .uses_dynamic_stack: false
    .vgpr_count:     61
    .vgpr_spill_count: 0
    .wavefront_size: 64
  - .agpr_count:     0
    .args:
      - .actual_access:  read_only
        .address_space:  global
        .offset:         0
        .size:           8
        .value_kind:     global_buffer
      - .actual_access:  read_only
        .address_space:  global
        .offset:         8
        .size:           8
        .value_kind:     global_buffer
      - .actual_access:  read_only
        .address_space:  global
        .offset:         16
        .size:           8
        .value_kind:     global_buffer
      - .actual_access:  write_only
        .address_space:  global
        .offset:         24
        .size:           8
        .value_kind:     global_buffer
      - .actual_access:  write_only
        .address_space:  global
        .offset:         32
        .size:           8
        .value_kind:     global_buffer
    .group_segment_fixed_size: 1072
    .kernarg_segment_align: 8
    .kernarg_segment_size: 40
    .language:       OpenCL C
    .language_version:
      - 2
      - 0
    .max_flat_workgroup_size: 768
    .name:           _Z7k3_histPKfPKiS0_PjPf
    .private_segment_fixed_size: 0
    .sgpr_count:     51
    .sgpr_spill_count: 0
    .symbol:         _Z7k3_histPKfPKiS0_PjPf.kd
    .uniform_work_group_size: 1
    .uses_dynamic_stack: false
    .vgpr_count:     64
    .vgpr_spill_count: 0
    .wavefront_size: 64
  - .agpr_count:     0
    .args:
      - .actual_access:  read_only
        .address_space:  global
        .offset:         0
        .size:           8
        .value_kind:     global_buffer
      - .actual_access:  write_only
        .address_space:  global
        .offset:         8
        .size:           8
        .value_kind:     global_buffer
    .group_segment_fixed_size: 8192
    .kernarg_segment_align: 8
    .kernarg_segment_size: 16
    .language:       OpenCL C
    .language_version:
      - 2
      - 0
    .max_flat_workgroup_size: 256
    .name:           _Z9k4_reducePKjP15HIP_vector_typeIjLj2EE
    .private_segment_fixed_size: 0
    .sgpr_count:     34
    .sgpr_spill_count: 0
    .symbol:         _Z9k4_reducePKjP15HIP_vector_typeIjLj2EE.kd
    .uniform_work_group_size: 1
    .uses_dynamic_stack: false
    .vgpr_count:     52
    .vgpr_spill_count: 0
    .wavefront_size: 64
  - .agpr_count:     0
    .args:
      - .actual_access:  read_only
        .address_space:  global
        .offset:         0
        .size:           8
        .value_kind:     global_buffer
      - .actual_access:  read_only
        .address_space:  global
        .offset:         8
        .size:           8
        .value_kind:     global_buffer
      - .actual_access:  read_only
        .address_space:  global
        .offset:         16
        .size:           8
        .value_kind:     global_buffer
      - .address_space:  global
        .offset:         24
        .size:           8
        .value_kind:     global_buffer
      - .actual_access:  write_only
        .address_space:  global
        .offset:         32
        .size:           8
        .value_kind:     global_buffer
      - .offset:         40
        .size:           4
        .value_kind:     hidden_block_count_x
      - .offset:         44
        .size:           4
        .value_kind:     hidden_block_count_y
      - .offset:         48
        .size:           4
        .value_kind:     hidden_block_count_z
      - .offset:         52
        .size:           2
        .value_kind:     hidden_group_size_x
      - .offset:         54
        .size:           2
        .value_kind:     hidden_group_size_y
      - .offset:         56
        .size:           2
        .value_kind:     hidden_group_size_z
      - .offset:         58
        .size:           2
        .value_kind:     hidden_remainder_x
      - .offset:         60
        .size:           2
        .value_kind:     hidden_remainder_y
      - .offset:         62
        .size:           2
        .value_kind:     hidden_remainder_z
      - .offset:         80
        .size:           8
        .value_kind:     hidden_global_offset_x
      - .offset:         88
        .size:           8
        .value_kind:     hidden_global_offset_y
      - .offset:         96
        .size:           8
        .value_kind:     hidden_global_offset_z
      - .offset:         104
        .size:           2
        .value_kind:     hidden_grid_dims
    .group_segment_fixed_size: 12544
    .kernarg_segment_align: 8
    .kernarg_segment_size: 296
    .language:       OpenCL C
    .language_version:
      - 2
      - 0
    .max_flat_workgroup_size: 1024
    .name:           _Z8k5_finalPK15HIP_vector_typeIjLj2EEPKfS4_PyPf
    .private_segment_fixed_size: 0
    .sgpr_count:     30
    .sgpr_spill_count: 0
    .symbol:         _Z8k5_finalPK15HIP_vector_typeIjLj2EEPKfS4_PyPf.kd
    .uniform_work_group_size: 1
    .uses_dynamic_stack: false
    .vgpr_count:     40
    .vgpr_spill_count: 0
    .wavefront_size: 64
